# expert weight conversion in grid barriers, front-loaded slots 21,21,14,14,14,12
# speedup vs baseline: 1.0051x; 1.0051x over previous
.Lhw_seam0:
	s_mov_b64 exec, -1
	v_readlane_b32 s2, v239, 0
	s_lshr_b32 s2, s2, 6
	s_add_i32 s2, s2, -1
	s_cmp_gt_u32 s2, 20
	s_cbranch_scc1 .Lhw_seam0_done
	s_add_i32 s2, s2, 0
	s_mul_i32 s2, s2, s74
	v_readlane_b32 s9, v239, 23
	s_lshr_b32 s9, s9, 3
	s_add_i32 s2, s2, s9
	s_cmp_gt_u32 s2, 24575
	s_cbranch_scc1 .Lhw_seam0_done
	v_mbcnt_lo_u32_b32 v178, -1, 0
	v_mbcnt_hi_u32_b32 v178, -1, v178
	v_and_b32_e32 v179, 60, v178
	v_lshlrev_b32_e32 v179, 10, v179
	v_and_b32_e32 v180, 3, v178
	v_lshl_or_b32 v179, v180, 4, v179
	v_add_u32_e32 v180, 0x400, v179
	v_add_u32_e32 v181, 0x800, v179
	v_add_u32_e32 v190, 0xc00, v179
	v_lshlrev_b32_e32 v178, 2, v178
	s_cmp_lt_u32 s2, 16384
	s_cbranch_scc0 .Lhw_dn_s0_0
	s_lshr_b32 s9, s2, 9
	s_bfe_u32 s32, s2, 0x40005
	s_and_b32 s53, s2, 31
	s_lshl_b32 s69, s9, 23
	s_lshl_b32 s100, s32, 19
	s_add_i32 s69, s69, s100
	s_lshl_b32 s100, s53, 8
	s_add_i32 s69, s69, s100
	s_lshl_b32 s98, s9, 11
	s_bfe_u32 s100, s53, 0x30001
	s_lshl_b32 s100, s100, 8
	s_add_i32 s98, s98, s100
	s_lshr_b32 s100, s53, 4
	s_lshl_b32 s100, s100, 7
	s_add_i32 s98, s98, s100
	s_and_b32 s100, s53, 1
	s_lshl_b32 s100, s100, 6
	s_add_i32 s98, s98, s100
	s_lshl_b32 s98, s98, 10
	s_lshl_b32 s100, s32, 6
	s_add_i32 s98, s98, s100
	s_add_i32 s98, s98, 0x2000000
	v_readlane_b32 s82, v239, 11
	v_readlane_b32 s83, v239, 12
	s_movk_i32 s89, 8192
	s_branch .Lhw_go_s0_0

.Lhw_go_s0_0:
	s_add_u32 s100, s82, s69
	s_addc_u32 s101, s83, 0
	v_readlane_b32 s82, v239, 44
	v_readlane_b32 s83, v239, 45
	s_add_u32 s82, s82, s98
	s_addc_u32 s83, s83, 0
	global_load_dword v34, v178, s[100:101] nt
	s_add_u32 s100, s100, s89
	s_addc_u32 s101, s101, 0
	global_load_dword v35, v178, s[100:101] nt
	s_add_u32 s100, s100, s89
	s_addc_u32 s101, s101, 0
	global_load_dword v36, v178, s[100:101] nt
	s_add_u32 s100, s100, s89
	s_addc_u32 s101, s101, 0
	global_load_dword v37, v178, s[100:101] nt
	s_add_u32 s100, s100, s89
	s_addc_u32 s101, s101, 0
	global_load_dword v38, v178, s[100:101] nt
	s_add_u32 s100, s100, s89
	s_addc_u32 s101, s101, 0
	global_load_dword v39, v178, s[100:101] nt
	s_add_u32 s100, s100, s89
	s_addc_u32 s101, s101, 0
	global_load_dword v40, v178, s[100:101] nt
	s_add_u32 s100, s100, s89
	s_addc_u32 s101, s101, 0
	global_load_dword v41, v178, s[100:101] nt
	s_add_u32 s100, s100, s89
	s_addc_u32 s101, s101, 0
	global_load_dword v42, v178, s[100:101] nt
	s_add_u32 s100, s100, s89
	s_addc_u32 s101, s101, 0
	global_load_dword v43, v178, s[100:101] nt
	s_add_u32 s100, s100, s89
	s_addc_u32 s101, s101, 0
	global_load_dword v44, v178, s[100:101] nt
	s_add_u32 s100, s100, s89
	s_addc_u32 s101, s101, 0
	global_load_dword v45, v178, s[100:101] nt
	s_add_u32 s100, s100, s89
	s_addc_u32 s101, s101, 0
	global_load_dword v46, v178, s[100:101] nt
	s_add_u32 s100, s100, s89
	s_addc_u32 s101, s101, 0
	global_load_dword v47, v178, s[100:101] nt
	s_add_u32 s100, s100, s89
	s_addc_u32 s101, s101, 0
	global_load_dword v48, v178, s[100:101] nt
	s_add_u32 s100, s100, s89
	s_addc_u32 s101, s101, 0
	global_load_dword v49, v178, s[100:101] nt
	s_add_u32 s100, s100, s89
	s_addc_u32 s101, s101, 0
	global_load_dword v50, v178, s[100:101] nt
	s_add_u32 s100, s100, s89
	s_addc_u32 s101, s101, 0
	global_load_dword v51, v178, s[100:101] nt
	s_add_u32 s100, s100, s89
	s_addc_u32 s101, s101, 0
	global_load_dword v52, v178, s[100:101] nt
	s_add_u32 s100, s100, s89
	s_addc_u32 s101, s101, 0
	global_load_dword v53, v178, s[100:101] nt
	s_add_u32 s100, s100, s89
	s_addc_u32 s101, s101, 0
	global_load_dword v54, v178, s[100:101] nt
	s_add_u32 s100, s100, s89
	s_addc_u32 s101, s101, 0
	global_load_dword v55, v178, s[100:101] nt
	s_add_u32 s100, s100, s89
	s_addc_u32 s101, s101, 0
	global_load_dword v56, v178, s[100:101] nt
	s_add_u32 s100, s100, s89
	s_addc_u32 s101, s101, 0
	global_load_dword v57, v178, s[100:101] nt
	s_add_u32 s100, s100, s89
	s_addc_u32 s101, s101, 0
	global_load_dword v58, v178, s[100:101] nt
	s_add_u32 s100, s100, s89
	s_addc_u32 s101, s101, 0
	global_load_dword v59, v178, s[100:101] nt
	s_add_u32 s100, s100, s89
	s_addc_u32 s101, s101, 0
	global_load_dword v60, v178, s[100:101] nt
	s_add_u32 s100, s100, s89
	s_addc_u32 s101, s101, 0
	global_load_dword v61, v178, s[100:101] nt
	s_add_u32 s100, s100, s89
	s_addc_u32 s101, s101, 0
	global_load_dword v62, v178, s[100:101] nt
	s_add_u32 s100, s100, s89
	s_addc_u32 s101, s101, 0
	global_load_dword v63, v178, s[100:101] nt
	s_add_u32 s100, s100, s89
	s_addc_u32 s101, s101, 0
	global_load_dword v64, v178, s[100:101] nt
	s_add_u32 s100, s100, s89
	s_addc_u32 s101, s101, 0
	global_load_dword v65, v178, s[100:101] nt
	s_add_u32 s100, s100, s89
	s_addc_u32 s101, s101, 0
	global_load_dword v66, v178, s[100:101] nt
	s_add_u32 s100, s100, s89
	s_addc_u32 s101, s101, 0
	global_load_dword v67, v178, s[100:101] nt
	s_add_u32 s100, s100, s89
	s_addc_u32 s101, s101, 0
	global_load_dword v68, v178, s[100:101] nt
	s_add_u32 s100, s100, s89
	s_addc_u32 s101, s101, 0
	global_load_dword v69, v178, s[100:101] nt
	s_add_u32 s100, s100, s89
	s_addc_u32 s101, s101, 0
	global_load_dword v70, v178, s[100:101] nt
	s_add_u32 s100, s100, s89
	s_addc_u32 s101, s101, 0
	global_load_dword v71, v178, s[100:101] nt
	s_add_u32 s100, s100, s89
	s_addc_u32 s101, s101, 0
	global_load_dword v72, v178, s[100:101] nt
	s_add_u32 s100, s100, s89
	s_addc_u32 s101, s101, 0
	global_load_dword v73, v178, s[100:101] nt
	s_add_u32 s100, s100, s89
	s_addc_u32 s101, s101, 0
	global_load_dword v74, v178, s[100:101] nt
	s_add_u32 s100, s100, s89
	s_addc_u32 s101, s101, 0
	global_load_dword v75, v178, s[100:101] nt
	s_add_u32 s100, s100, s89
	s_addc_u32 s101, s101, 0
	global_load_dword v76, v178, s[100:101] nt
	s_add_u32 s100, s100, s89
	s_addc_u32 s101, s101, 0
	global_load_dword v77, v178, s[100:101] nt
	s_add_u32 s100, s100, s89
	s_addc_u32 s101, s101, 0
	global_load_dword v78, v178, s[100:101] nt
	s_add_u32 s100, s100, s89
	s_addc_u32 s101, s101, 0
	global_load_dword v79, v178, s[100:101] nt
	s_add_u32 s100, s100, s89
	s_addc_u32 s101, s101, 0
	global_load_dword v80, v178, s[100:101] nt
	s_add_u32 s100, s100, s89
	s_addc_u32 s101, s101, 0
	global_load_dword v81, v178, s[100:101] nt
	s_add_u32 s100, s100, s89
	s_addc_u32 s101, s101, 0
	global_load_dword v82, v178, s[100:101] nt
	s_add_u32 s100, s100, s89
	s_addc_u32 s101, s101, 0
	global_load_dword v83, v178, s[100:101] nt
	s_add_u32 s100, s100, s89
	s_addc_u32 s101, s101, 0
	global_load_dword v84, v178, s[100:101] nt
	s_add_u32 s100, s100, s89
	s_addc_u32 s101, s101, 0
	global_load_dword v85, v178, s[100:101] nt
	s_add_u32 s100, s100, s89
	s_addc_u32 s101, s101, 0
	global_load_dword v86, v178, s[100:101] nt
	s_add_u32 s100, s100, s89
	s_addc_u32 s101, s101, 0
	global_load_dword v87, v178, s[100:101] nt
	s_add_u32 s100, s100, s89
	s_addc_u32 s101, s101, 0
	global_load_dword v88, v178, s[100:101] nt
	s_add_u32 s100, s100, s89
	s_addc_u32 s101, s101, 0
	global_load_dword v89, v178, s[100:101] nt
	s_add_u32 s100, s100, s89
	s_addc_u32 s101, s101, 0
	global_load_dword v90, v178, s[100:101] nt
	s_add_u32 s100, s100, s89
	s_addc_u32 s101, s101, 0
	global_load_dword v91, v178, s[100:101] nt
	s_add_u32 s100, s100, s89
	s_addc_u32 s101, s101, 0
	global_load_dword v92, v178, s[100:101] nt
	s_add_u32 s100, s100, s89
	s_addc_u32 s101, s101, 0
	global_load_dword v93, v178, s[100:101] nt
	s_add_u32 s100, s100, s89
	s_addc_u32 s101, s101, 0
	global_load_dword v94, v178, s[100:101] nt
	s_add_u32 s100, s100, s89
	s_addc_u32 s101, s101, 0
	global_load_dword v95, v178, s[100:101] nt
	s_add_u32 s100, s100, s89
	s_addc_u32 s101, s101, 0
	global_load_dword v96, v178, s[100:101] nt
	s_add_u32 s100, s100, s89
	s_addc_u32 s101, s101, 0
	global_load_dword v97, v178, s[100:101] nt
	s_add_u32 s100, s100, s89
	s_addc_u32 s101, s101, 0
	s_waitcnt vmcnt(48)
	v_mul_f32_e32 v34, 0x42000000, v34
	v_mul_f32_e32 v35, 0x42000000, v35
	v_mul_f32_e32 v36, 0x42000000, v36
	v_mul_f32_e32 v37, 0x42000000, v37
	v_mul_f32_e32 v38, 0x42000000, v38
	v_mul_f32_e32 v39, 0x42000000, v39
	v_mul_f32_e32 v40, 0x42000000, v40
	v_mul_f32_e32 v41, 0x42000000, v41
	v_mul_f32_e32 v42, 0x42000000, v42
	v_mul_f32_e32 v43, 0x42000000, v43
	v_mul_f32_e32 v44, 0x42000000, v44
	v_mul_f32_e32 v45, 0x42000000, v45
	v_mul_f32_e32 v46, 0x42000000, v46
	v_mul_f32_e32 v47, 0x42000000, v47
	v_mul_f32_e32 v48, 0x42000000, v48
	v_mul_f32_e32 v49, 0x42000000, v49
	v_cvt_pk_fp8_f32 v154, v34, v35
	v_cvt_pk_fp8_f32 v155, v38, v39
	v_cvt_pk_fp8_f32 v156, v42, v43
	v_cvt_pk_fp8_f32 v157, v46, v47
	v_cvt_pk_fp8_f32 v154, v36, v37 op_sel:[0,0,1]
	v_cvt_pk_fp8_f32 v155, v40, v41 op_sel:[0,0,1]
	v_cvt_pk_fp8_f32 v156, v44, v45 op_sel:[0,0,1]
	v_cvt_pk_fp8_f32 v157, v48, v49 op_sel:[0,0,1]
	s_waitcnt vmcnt(32)
	v_mul_f32_e32 v50, 0x42000000, v50
	v_mul_f32_e32 v51, 0x42000000, v51
	v_mul_f32_e32 v52, 0x42000000, v52
	v_mul_f32_e32 v53, 0x42000000, v53
	v_mul_f32_e32 v54, 0x42000000, v54
	v_mul_f32_e32 v55, 0x42000000, v55
	v_mul_f32_e32 v56, 0x42000000, v56
	v_mul_f32_e32 v57, 0x42000000, v57
	v_mul_f32_e32 v58, 0x42000000, v58
	v_mul_f32_e32 v59, 0x42000000, v59
	v_mul_f32_e32 v60, 0x42000000, v60
	v_mul_f32_e32 v61, 0x42000000, v61
	v_mul_f32_e32 v62, 0x42000000, v62
	v_mul_f32_e32 v63, 0x42000000, v63
	v_mul_f32_e32 v64, 0x42000000, v64
	v_mul_f32_e32 v65, 0x42000000, v65
	v_cvt_pk_fp8_f32 v158, v50, v51
	v_cvt_pk_fp8_f32 v159, v54, v55
	v_cvt_pk_fp8_f32 v160, v58, v59
	v_cvt_pk_fp8_f32 v161, v62, v63
	v_cvt_pk_fp8_f32 v158, v52, v53 op_sel:[0,0,1]
	v_cvt_pk_fp8_f32 v159, v56, v57 op_sel:[0,0,1]
	v_cvt_pk_fp8_f32 v160, v60, v61 op_sel:[0,0,1]
	v_cvt_pk_fp8_f32 v161, v64, v65 op_sel:[0,0,1]
	s_waitcnt vmcnt(16)
	v_mul_f32_e32 v66, 0x42000000, v66
	v_mul_f32_e32 v67, 0x42000000, v67
	v_mul_f32_e32 v68, 0x42000000, v68
	v_mul_f32_e32 v69, 0x42000000, v69
	v_mul_f32_e32 v70, 0x42000000, v70
	v_mul_f32_e32 v71, 0x42000000, v71
	v_mul_f32_e32 v72, 0x42000000, v72
	v_mul_f32_e32 v73, 0x42000000, v73
	v_mul_f32_e32 v74, 0x42000000, v74
	v_mul_f32_e32 v75, 0x42000000, v75
	v_mul_f32_e32 v76, 0x42000000, v76
	v_mul_f32_e32 v77, 0x42000000, v77
	v_mul_f32_e32 v78, 0x42000000, v78
	v_mul_f32_e32 v79, 0x42000000, v79
	v_mul_f32_e32 v80, 0x42000000, v80
	v_mul_f32_e32 v81, 0x42000000, v81
	v_cvt_pk_fp8_f32 v162, v66, v67
	v_cvt_pk_fp8_f32 v163, v70, v71
	v_cvt_pk_fp8_f32 v164, v74, v75
	v_cvt_pk_fp8_f32 v165, v78, v79
	v_cvt_pk_fp8_f32 v162, v68, v69 op_sel:[0,0,1]
	v_cvt_pk_fp8_f32 v163, v72, v73 op_sel:[0,0,1]
	v_cvt_pk_fp8_f32 v164, v76, v77 op_sel:[0,0,1]
	v_cvt_pk_fp8_f32 v165, v80, v81 op_sel:[0,0,1]
	s_waitcnt vmcnt(0)
	v_mul_f32_e32 v82, 0x42000000, v82
	v_mul_f32_e32 v83, 0x42000000, v83
	v_mul_f32_e32 v84, 0x42000000, v84
	v_mul_f32_e32 v85, 0x42000000, v85
	v_mul_f32_e32 v86, 0x42000000, v86
	v_mul_f32_e32 v87, 0x42000000, v87
	v_mul_f32_e32 v88, 0x42000000, v88
	v_mul_f32_e32 v89, 0x42000000, v89
	v_mul_f32_e32 v90, 0x42000000, v90
	v_mul_f32_e32 v91, 0x42000000, v91
	v_mul_f32_e32 v92, 0x42000000, v92
	v_mul_f32_e32 v93, 0x42000000, v93
	v_mul_f32_e32 v94, 0x42000000, v94
	v_mul_f32_e32 v95, 0x42000000, v95
	v_mul_f32_e32 v96, 0x42000000, v96
	v_mul_f32_e32 v97, 0x42000000, v97
	v_cvt_pk_fp8_f32 v166, v82, v83
	v_cvt_pk_fp8_f32 v167, v86, v87
	v_cvt_pk_fp8_f32 v168, v90, v91
	v_cvt_pk_fp8_f32 v169, v94, v95
	v_cvt_pk_fp8_f32 v166, v84, v85 op_sel:[0,0,1]
	v_cvt_pk_fp8_f32 v167, v88, v89 op_sel:[0,0,1]
	v_cvt_pk_fp8_f32 v168, v92, v93 op_sel:[0,0,1]
	v_cvt_pk_fp8_f32 v169, v96, v97 op_sel:[0,0,1]
	s_mov_b32 vcc_lo, 0xaaaaaaaa
	s_mov_b32 vcc_hi, 0xaaaaaaaa
	s_nop 1
	v_cndmask_b32_dpp v170, v154, v158, vcc quad_perm:[1,0,3,2] row_mask:0xf bank_mask:0xf
	v_cndmask_b32_dpp v174, v162, v166, vcc quad_perm:[1,0,3,2] row_mask:0xf bank_mask:0xf
	v_cndmask_b32_dpp v171, v155, v159, vcc quad_perm:[1,0,3,2] row_mask:0xf bank_mask:0xf
	v_cndmask_b32_dpp v175, v163, v167, vcc quad_perm:[1,0,3,2] row_mask:0xf bank_mask:0xf
	v_cndmask_b32_dpp v172, v156, v160, vcc quad_perm:[1,0,3,2] row_mask:0xf bank_mask:0xf
	v_cndmask_b32_dpp v176, v164, v168, vcc quad_perm:[1,0,3,2] row_mask:0xf bank_mask:0xf
	v_cndmask_b32_dpp v173, v157, v161, vcc quad_perm:[1,0,3,2] row_mask:0xf bank_mask:0xf
	v_cndmask_b32_dpp v177, v165, v169, vcc quad_perm:[1,0,3,2] row_mask:0xf bank_mask:0xf
	s_mov_b32 vcc_lo, 0x55555555
	s_mov_b32 vcc_hi, 0x55555555
	s_nop 1
	v_cndmask_b32_dpp v154, v158, v154, vcc quad_perm:[1,0,3,2] row_mask:0xf bank_mask:0xf
	v_cndmask_b32_dpp v162, v166, v162, vcc quad_perm:[1,0,3,2] row_mask:0xf bank_mask:0xf
	v_cndmask_b32_dpp v155, v159, v155, vcc quad_perm:[1,0,3,2] row_mask:0xf bank_mask:0xf
	v_cndmask_b32_dpp v163, v167, v163, vcc quad_perm:[1,0,3,2] row_mask:0xf bank_mask:0xf
	v_cndmask_b32_dpp v156, v160, v156, vcc quad_perm:[1,0,3,2] row_mask:0xf bank_mask:0xf
	v_cndmask_b32_dpp v164, v168, v164, vcc quad_perm:[1,0,3,2] row_mask:0xf bank_mask:0xf
	v_cndmask_b32_dpp v157, v161, v157, vcc quad_perm:[1,0,3,2] row_mask:0xf bank_mask:0xf
	v_cndmask_b32_dpp v165, v169, v165, vcc quad_perm:[1,0,3,2] row_mask:0xf bank_mask:0xf
	s_mov_b32 vcc_lo, 0xcccccccc
	s_mov_b32 vcc_hi, 0xcccccccc
	s_nop 1
	v_cndmask_b32_dpp v158, v154, v162, vcc quad_perm:[2,3,0,1] row_mask:0xf bank_mask:0xf
	v_cndmask_b32_dpp v166, v170, v174, vcc quad_perm:[2,3,0,1] row_mask:0xf bank_mask:0xf
	v_cndmask_b32_dpp v159, v155, v163, vcc quad_perm:[2,3,0,1] row_mask:0xf bank_mask:0xf
	v_cndmask_b32_dpp v167, v171, v175, vcc quad_perm:[2,3,0,1] row_mask:0xf bank_mask:0xf
	v_cndmask_b32_dpp v160, v156, v164, vcc quad_perm:[2,3,0,1] row_mask:0xf bank_mask:0xf
	v_cndmask_b32_dpp v168, v172, v176, vcc quad_perm:[2,3,0,1] row_mask:0xf bank_mask:0xf
	v_cndmask_b32_dpp v161, v157, v165, vcc quad_perm:[2,3,0,1] row_mask:0xf bank_mask:0xf
	v_cndmask_b32_dpp v169, v173, v177, vcc quad_perm:[2,3,0,1] row_mask:0xf bank_mask:0xf
	s_mov_b32 vcc_lo, 0x33333333
	s_mov_b32 vcc_hi, 0x33333333
	s_nop 1
	v_cndmask_b32_dpp v154, v162, v154, vcc quad_perm:[2,3,0,1] row_mask:0xf bank_mask:0xf
	v_cndmask_b32_dpp v170, v174, v170, vcc quad_perm:[2,3,0,1] row_mask:0xf bank_mask:0xf
	v_cndmask_b32_dpp v155, v163, v155, vcc quad_perm:[2,3,0,1] row_mask:0xf bank_mask:0xf
	v_cndmask_b32_dpp v171, v175, v171, vcc quad_perm:[2,3,0,1] row_mask:0xf bank_mask:0xf
	v_cndmask_b32_dpp v156, v164, v156, vcc quad_perm:[2,3,0,1] row_mask:0xf bank_mask:0xf
	v_cndmask_b32_dpp v172, v176, v172, vcc quad_perm:[2,3,0,1] row_mask:0xf bank_mask:0xf
	v_cndmask_b32_dpp v157, v165, v157, vcc quad_perm:[2,3,0,1] row_mask:0xf bank_mask:0xf
	v_cndmask_b32_dpp v173, v177, v173, vcc quad_perm:[2,3,0,1] row_mask:0xf bank_mask:0xf
	global_store_dwordx4 v179, v[154:157], s[82:83] nt
	global_store_dwordx4 v180, v[170:173], s[82:83] nt
	global_store_dwordx4 v181, v[158:161], s[82:83] nt
	global_store_dwordx4 v190, v[166:169], s[82:83] nt
	v_readlane_b32 s2, v239, 0
	s_lshr_b32 s2, s2, 6
	s_add_i32 s2, s2, 6
	s_cmp_gt_u32 s2, 20
	s_cbranch_scc1 .Lhw_seam0_done
	s_add_i32 s2, s2, 0
	s_mul_i32 s2, s2, s74
	v_readlane_b32 s9, v239, 23
	s_lshr_b32 s9, s9, 3
	s_add_i32 s2, s2, s9
	s_cmp_gt_u32 s2, 24575
	s_cbranch_scc1 .Lhw_seam0_done
	v_mbcnt_lo_u32_b32 v178, -1, 0
	v_mbcnt_hi_u32_b32 v178, -1, v178
	v_and_b32_e32 v179, 60, v178
	v_lshlrev_b32_e32 v179, 10, v179
	v_and_b32_e32 v180, 3, v178
	v_lshl_or_b32 v179, v180, 4, v179
	v_add_u32_e32 v180, 0x400, v179
	v_add_u32_e32 v181, 0x800, v179
	v_add_u32_e32 v190, 0xc00, v179
	v_lshlrev_b32_e32 v178, 2, v178
	s_cmp_lt_u32 s2, 16384
	s_cbranch_scc0 .Lhw_dn_s0_1
	s_lshr_b32 s9, s2, 9
	s_bfe_u32 s32, s2, 0x40005
	s_and_b32 s53, s2, 31
	s_lshl_b32 s69, s9, 23
	s_lshl_b32 s100, s32, 19
	s_add_i32 s69, s69, s100
	s_lshl_b32 s100, s53, 8
	s_add_i32 s69, s69, s100
	s_lshl_b32 s98, s9, 11
	s_bfe_u32 s100, s53, 0x30001
	s_lshl_b32 s100, s100, 8
	s_add_i32 s98, s98, s100
	s_lshr_b32 s100, s53, 4
	s_lshl_b32 s100, s100, 7
	s_add_i32 s98, s98, s100
	s_and_b32 s100, s53, 1
	s_lshl_b32 s100, s100, 6
	s_add_i32 s98, s98, s100
	s_lshl_b32 s98, s98, 10
	s_lshl_b32 s100, s32, 6
	s_add_i32 s98, s98, s100
	s_add_i32 s98, s98, 0x2000000
	v_readlane_b32 s82, v239, 11
	v_readlane_b32 s83, v239, 12
	s_movk_i32 s89, 8192
	s_branch .Lhw_go_s0_1

.Lhw_go_s0_1:
	s_add_u32 s100, s82, s69
	s_addc_u32 s101, s83, 0
	v_readlane_b32 s82, v239, 44
	v_readlane_b32 s83, v239, 45
	s_add_u32 s82, s82, s98
	s_addc_u32 s83, s83, 0
	global_load_dword v34, v178, s[100:101] nt
	s_add_u32 s100, s100, s89
	s_addc_u32 s101, s101, 0
	global_load_dword v35, v178, s[100:101] nt
	s_add_u32 s100, s100, s89
	s_addc_u32 s101, s101, 0
	global_load_dword v36, v178, s[100:101] nt
	s_add_u32 s100, s100, s89
	s_addc_u32 s101, s101, 0
	global_load_dword v37, v178, s[100:101] nt
	s_add_u32 s100, s100, s89
	s_addc_u32 s101, s101, 0
	global_load_dword v38, v178, s[100:101] nt
	s_add_u32 s100, s100, s89
	s_addc_u32 s101, s101, 0
	global_load_dword v39, v178, s[100:101] nt
	s_add_u32 s100, s100, s89
	s_addc_u32 s101, s101, 0
	global_load_dword v40, v178, s[100:101] nt
	s_add_u32 s100, s100, s89
	s_addc_u32 s101, s101, 0
	global_load_dword v41, v178, s[100:101] nt
	s_add_u32 s100, s100, s89
	s_addc_u32 s101, s101, 0
	global_load_dword v42, v178, s[100:101] nt
	s_add_u32 s100, s100, s89
	s_addc_u32 s101, s101, 0
	global_load_dword v43, v178, s[100:101] nt
	s_add_u32 s100, s100, s89
	s_addc_u32 s101, s101, 0
	global_load_dword v44, v178, s[100:101] nt
	s_add_u32 s100, s100, s89
	s_addc_u32 s101, s101, 0
	global_load_dword v45, v178, s[100:101] nt
	s_add_u32 s100, s100, s89
	s_addc_u32 s101, s101, 0
	global_load_dword v46, v178, s[100:101] nt
	s_add_u32 s100, s100, s89
	s_addc_u32 s101, s101, 0
	global_load_dword v47, v178, s[100:101] nt
	s_add_u32 s100, s100, s89
	s_addc_u32 s101, s101, 0
	global_load_dword v48, v178, s[100:101] nt
	s_add_u32 s100, s100, s89
	s_addc_u32 s101, s101, 0
	global_load_dword v49, v178, s[100:101] nt
	s_add_u32 s100, s100, s89
	s_addc_u32 s101, s101, 0
	global_load_dword v50, v178, s[100:101] nt
	s_add_u32 s100, s100, s89
	s_addc_u32 s101, s101, 0
	global_load_dword v51, v178, s[100:101] nt
	s_add_u32 s100, s100, s89
	s_addc_u32 s101, s101, 0
	global_load_dword v52, v178, s[100:101] nt
	s_add_u32 s100, s100, s89
	s_addc_u32 s101, s101, 0
	global_load_dword v53, v178, s[100:101] nt
	s_add_u32 s100, s100, s89
	s_addc_u32 s101, s101, 0
	global_load_dword v54, v178, s[100:101] nt
	s_add_u32 s100, s100, s89
	s_addc_u32 s101, s101, 0
	global_load_dword v55, v178, s[100:101] nt
	s_add_u32 s100, s100, s89
	s_addc_u32 s101, s101, 0
	global_load_dword v56, v178, s[100:101] nt
	s_add_u32 s100, s100, s89
	s_addc_u32 s101, s101, 0
	global_load_dword v57, v178, s[100:101] nt
	s_add_u32 s100, s100, s89
	s_addc_u32 s101, s101, 0
	global_load_dword v58, v178, s[100:101] nt
	s_add_u32 s100, s100, s89
	s_addc_u32 s101, s101, 0
	global_load_dword v59, v178, s[100:101] nt
	s_add_u32 s100, s100, s89
	s_addc_u32 s101, s101, 0
	global_load_dword v60, v178, s[100:101] nt
	s_add_u32 s100, s100, s89
	s_addc_u32 s101, s101, 0
	global_load_dword v61, v178, s[100:101] nt
	s_add_u32 s100, s100, s89
	s_addc_u32 s101, s101, 0
	global_load_dword v62, v178, s[100:101] nt
	s_add_u32 s100, s100, s89
	s_addc_u32 s101, s101, 0
	global_load_dword v63, v178, s[100:101] nt
	s_add_u32 s100, s100, s89
	s_addc_u32 s101, s101, 0
	global_load_dword v64, v178, s[100:101] nt
	s_add_u32 s100, s100, s89
	s_addc_u32 s101, s101, 0
	global_load_dword v65, v178, s[100:101] nt
	s_add_u32 s100, s100, s89
	s_addc_u32 s101, s101, 0
	global_load_dword v66, v178, s[100:101] nt
	s_add_u32 s100, s100, s89
	s_addc_u32 s101, s101, 0
	global_load_dword v67, v178, s[100:101] nt
	s_add_u32 s100, s100, s89
	s_addc_u32 s101, s101, 0
	global_load_dword v68, v178, s[100:101] nt
	s_add_u32 s100, s100, s89
	s_addc_u32 s101, s101, 0
	global_load_dword v69, v178, s[100:101] nt
	s_add_u32 s100, s100, s89
	s_addc_u32 s101, s101, 0
	global_load_dword v70, v178, s[100:101] nt
	s_add_u32 s100, s100, s89
	s_addc_u32 s101, s101, 0
	global_load_dword v71, v178, s[100:101] nt
	s_add_u32 s100, s100, s89
	s_addc_u32 s101, s101, 0
	global_load_dword v72, v178, s[100:101] nt
	s_add_u32 s100, s100, s89
	s_addc_u32 s101, s101, 0
	global_load_dword v73, v178, s[100:101] nt
	s_add_u32 s100, s100, s89
	s_addc_u32 s101, s101, 0
	global_load_dword v74, v178, s[100:101] nt
	s_add_u32 s100, s100, s89
	s_addc_u32 s101, s101, 0
	global_load_dword v75, v178, s[100:101] nt
	s_add_u32 s100, s100, s89
	s_addc_u32 s101, s101, 0
	global_load_dword v76, v178, s[100:101] nt
	s_add_u32 s100, s100, s89
	s_addc_u32 s101, s101, 0
	global_load_dword v77, v178, s[100:101] nt
	s_add_u32 s100, s100, s89
	s_addc_u32 s101, s101, 0
	global_load_dword v78, v178, s[100:101] nt
	s_add_u32 s100, s100, s89
	s_addc_u32 s101, s101, 0
	global_load_dword v79, v178, s[100:101] nt
	s_add_u32 s100, s100, s89
	s_addc_u32 s101, s101, 0
	global_load_dword v80, v178, s[100:101] nt
	s_add_u32 s100, s100, s89
	s_addc_u32 s101, s101, 0
	global_load_dword v81, v178, s[100:101] nt
	s_add_u32 s100, s100, s89
	s_addc_u32 s101, s101, 0
	global_load_dword v82, v178, s[100:101] nt
	s_add_u32 s100, s100, s89
	s_addc_u32 s101, s101, 0
	global_load_dword v83, v178, s[100:101] nt
	s_add_u32 s100, s100, s89
	s_addc_u32 s101, s101, 0
	global_load_dword v84, v178, s[100:101] nt
	s_add_u32 s100, s100, s89
	s_addc_u32 s101, s101, 0
	global_load_dword v85, v178, s[100:101] nt
	s_add_u32 s100, s100, s89
	s_addc_u32 s101, s101, 0
	global_load_dword v86, v178, s[100:101] nt
	s_add_u32 s100, s100, s89
	s_addc_u32 s101, s101, 0
	global_load_dword v87, v178, s[100:101] nt
	s_add_u32 s100, s100, s89
	s_addc_u32 s101, s101, 0
	global_load_dword v88, v178, s[100:101] nt
	s_add_u32 s100, s100, s89
	s_addc_u32 s101, s101, 0
	global_load_dword v89, v178, s[100:101] nt
	s_add_u32 s100, s100, s89
	s_addc_u32 s101, s101, 0
	global_load_dword v90, v178, s[100:101] nt
	s_add_u32 s100, s100, s89
	s_addc_u32 s101, s101, 0
	global_load_dword v91, v178, s[100:101] nt
	s_add_u32 s100, s100, s89
	s_addc_u32 s101, s101, 0
	global_load_dword v92, v178, s[100:101] nt
	s_add_u32 s100, s100, s89
	s_addc_u32 s101, s101, 0
	global_load_dword v93, v178, s[100:101] nt
	s_add_u32 s100, s100, s89
	s_addc_u32 s101, s101, 0
	global_load_dword v94, v178, s[100:101] nt
	s_add_u32 s100, s100, s89
	s_addc_u32 s101, s101, 0
	global_load_dword v95, v178, s[100:101] nt
	s_add_u32 s100, s100, s89
	s_addc_u32 s101, s101, 0
	global_load_dword v96, v178, s[100:101] nt
	s_add_u32 s100, s100, s89
	s_addc_u32 s101, s101, 0
	global_load_dword v97, v178, s[100:101] nt
	s_add_u32 s100, s100, s89
	s_addc_u32 s101, s101, 0
	s_waitcnt vmcnt(48)
	v_mul_f32_e32 v34, 0x42000000, v34
	v_mul_f32_e32 v35, 0x42000000, v35
	v_mul_f32_e32 v36, 0x42000000, v36
	v_mul_f32_e32 v37, 0x42000000, v37
	v_mul_f32_e32 v38, 0x42000000, v38
	v_mul_f32_e32 v39, 0x42000000, v39
	v_mul_f32_e32 v40, 0x42000000, v40
	v_mul_f32_e32 v41, 0x42000000, v41
	v_mul_f32_e32 v42, 0x42000000, v42
	v_mul_f32_e32 v43, 0x42000000, v43
	v_mul_f32_e32 v44, 0x42000000, v44
	v_mul_f32_e32 v45, 0x42000000, v45
	v_mul_f32_e32 v46, 0x42000000, v46
	v_mul_f32_e32 v47, 0x42000000, v47
	v_mul_f32_e32 v48, 0x42000000, v48
	v_mul_f32_e32 v49, 0x42000000, v49
	v_cvt_pk_fp8_f32 v154, v34, v35
	v_cvt_pk_fp8_f32 v155, v38, v39
	v_cvt_pk_fp8_f32 v156, v42, v43
	v_cvt_pk_fp8_f32 v157, v46, v47
	v_cvt_pk_fp8_f32 v154, v36, v37 op_sel:[0,0,1]
	v_cvt_pk_fp8_f32 v155, v40, v41 op_sel:[0,0,1]
	v_cvt_pk_fp8_f32 v156, v44, v45 op_sel:[0,0,1]
	v_cvt_pk_fp8_f32 v157, v48, v49 op_sel:[0,0,1]
	s_waitcnt vmcnt(32)
	v_mul_f32_e32 v50, 0x42000000, v50
	v_mul_f32_e32 v51, 0x42000000, v51
	v_mul_f32_e32 v52, 0x42000000, v52
	v_mul_f32_e32 v53, 0x42000000, v53
	v_mul_f32_e32 v54, 0x42000000, v54
	v_mul_f32_e32 v55, 0x42000000, v55
	v_mul_f32_e32 v56, 0x42000000, v56
	v_mul_f32_e32 v57, 0x42000000, v57
	v_mul_f32_e32 v58, 0x42000000, v58
	v_mul_f32_e32 v59, 0x42000000, v59
	v_mul_f32_e32 v60, 0x42000000, v60
	v_mul_f32_e32 v61, 0x42000000, v61
	v_mul_f32_e32 v62, 0x42000000, v62
	v_mul_f32_e32 v63, 0x42000000, v63
	v_mul_f32_e32 v64, 0x42000000, v64
	v_mul_f32_e32 v65, 0x42000000, v65
	v_cvt_pk_fp8_f32 v158, v50, v51
	v_cvt_pk_fp8_f32 v159, v54, v55
	v_cvt_pk_fp8_f32 v160, v58, v59
	v_cvt_pk_fp8_f32 v161, v62, v63
	v_cvt_pk_fp8_f32 v158, v52, v53 op_sel:[0,0,1]
	v_cvt_pk_fp8_f32 v159, v56, v57 op_sel:[0,0,1]
	v_cvt_pk_fp8_f32 v160, v60, v61 op_sel:[0,0,1]
	v_cvt_pk_fp8_f32 v161, v64, v65 op_sel:[0,0,1]
	s_waitcnt vmcnt(16)
	v_mul_f32_e32 v66, 0x42000000, v66
	v_mul_f32_e32 v67, 0x42000000, v67
	v_mul_f32_e32 v68, 0x42000000, v68
	v_mul_f32_e32 v69, 0x42000000, v69
	v_mul_f32_e32 v70, 0x42000000, v70
	v_mul_f32_e32 v71, 0x42000000, v71
	v_mul_f32_e32 v72, 0x42000000, v72
	v_mul_f32_e32 v73, 0x42000000, v73
	v_mul_f32_e32 v74, 0x42000000, v74
	v_mul_f32_e32 v75, 0x42000000, v75
	v_mul_f32_e32 v76, 0x42000000, v76
	v_mul_f32_e32 v77, 0x42000000, v77
	v_mul_f32_e32 v78, 0x42000000, v78
	v_mul_f32_e32 v79, 0x42000000, v79
	v_mul_f32_e32 v80, 0x42000000, v80
	v_mul_f32_e32 v81, 0x42000000, v81
	v_cvt_pk_fp8_f32 v162, v66, v67
	v_cvt_pk_fp8_f32 v163, v70, v71
	v_cvt_pk_fp8_f32 v164, v74, v75
	v_cvt_pk_fp8_f32 v165, v78, v79
	v_cvt_pk_fp8_f32 v162, v68, v69 op_sel:[0,0,1]
	v_cvt_pk_fp8_f32 v163, v72, v73 op_sel:[0,0,1]
	v_cvt_pk_fp8_f32 v164, v76, v77 op_sel:[0,0,1]
	v_cvt_pk_fp8_f32 v165, v80, v81 op_sel:[0,0,1]
	s_waitcnt vmcnt(0)
	v_mul_f32_e32 v82, 0x42000000, v82
	v_mul_f32_e32 v83, 0x42000000, v83
	v_mul_f32_e32 v84, 0x42000000, v84
	v_mul_f32_e32 v85, 0x42000000, v85
	v_mul_f32_e32 v86, 0x42000000, v86
	v_mul_f32_e32 v87, 0x42000000, v87
	v_mul_f32_e32 v88, 0x42000000, v88
	v_mul_f32_e32 v89, 0x42000000, v89
	v_mul_f32_e32 v90, 0x42000000, v90
	v_mul_f32_e32 v91, 0x42000000, v91
	v_mul_f32_e32 v92, 0x42000000, v92
	v_mul_f32_e32 v93, 0x42000000, v93
	v_mul_f32_e32 v94, 0x42000000, v94
	v_mul_f32_e32 v95, 0x42000000, v95
	v_mul_f32_e32 v96, 0x42000000, v96
	v_mul_f32_e32 v97, 0x42000000, v97
	v_cvt_pk_fp8_f32 v166, v82, v83
	v_cvt_pk_fp8_f32 v167, v86, v87
	v_cvt_pk_fp8_f32 v168, v90, v91
	v_cvt_pk_fp8_f32 v169, v94, v95
	v_cvt_pk_fp8_f32 v166, v84, v85 op_sel:[0,0,1]
	v_cvt_pk_fp8_f32 v167, v88, v89 op_sel:[0,0,1]
	v_cvt_pk_fp8_f32 v168, v92, v93 op_sel:[0,0,1]
	v_cvt_pk_fp8_f32 v169, v96, v97 op_sel:[0,0,1]
	s_mov_b32 vcc_lo, 0xaaaaaaaa
	s_mov_b32 vcc_hi, 0xaaaaaaaa
	s_nop 1
	v_cndmask_b32_dpp v170, v154, v158, vcc quad_perm:[1,0,3,2] row_mask:0xf bank_mask:0xf
	v_cndmask_b32_dpp v174, v162, v166, vcc quad_perm:[1,0,3,2] row_mask:0xf bank_mask:0xf
	v_cndmask_b32_dpp v171, v155, v159, vcc quad_perm:[1,0,3,2] row_mask:0xf bank_mask:0xf
	v_cndmask_b32_dpp v175, v163, v167, vcc quad_perm:[1,0,3,2] row_mask:0xf bank_mask:0xf
	v_cndmask_b32_dpp v172, v156, v160, vcc quad_perm:[1,0,3,2] row_mask:0xf bank_mask:0xf
	v_cndmask_b32_dpp v176, v164, v168, vcc quad_perm:[1,0,3,2] row_mask:0xf bank_mask:0xf
	v_cndmask_b32_dpp v173, v157, v161, vcc quad_perm:[1,0,3,2] row_mask:0xf bank_mask:0xf
	v_cndmask_b32_dpp v177, v165, v169, vcc quad_perm:[1,0,3,2] row_mask:0xf bank_mask:0xf
	s_mov_b32 vcc_lo, 0x55555555
	s_mov_b32 vcc_hi, 0x55555555
	s_nop 1
	v_cndmask_b32_dpp v154, v158, v154, vcc quad_perm:[1,0,3,2] row_mask:0xf bank_mask:0xf
	v_cndmask_b32_dpp v162, v166, v162, vcc quad_perm:[1,0,3,2] row_mask:0xf bank_mask:0xf
	v_cndmask_b32_dpp v155, v159, v155, vcc quad_perm:[1,0,3,2] row_mask:0xf bank_mask:0xf
	v_cndmask_b32_dpp v163, v167, v163, vcc quad_perm:[1,0,3,2] row_mask:0xf bank_mask:0xf
	v_cndmask_b32_dpp v156, v160, v156, vcc quad_perm:[1,0,3,2] row_mask:0xf bank_mask:0xf
	v_cndmask_b32_dpp v164, v168, v164, vcc quad_perm:[1,0,3,2] row_mask:0xf bank_mask:0xf
	v_cndmask_b32_dpp v157, v161, v157, vcc quad_perm:[1,0,3,2] row_mask:0xf bank_mask:0xf
	v_cndmask_b32_dpp v165, v169, v165, vcc quad_perm:[1,0,3,2] row_mask:0xf bank_mask:0xf
	s_mov_b32 vcc_lo, 0xcccccccc
	s_mov_b32 vcc_hi, 0xcccccccc
	s_nop 1
	v_cndmask_b32_dpp v158, v154, v162, vcc quad_perm:[2,3,0,1] row_mask:0xf bank_mask:0xf
	v_cndmask_b32_dpp v166, v170, v174, vcc quad_perm:[2,3,0,1] row_mask:0xf bank_mask:0xf
	v_cndmask_b32_dpp v159, v155, v163, vcc quad_perm:[2,3,0,1] row_mask:0xf bank_mask:0xf
	v_cndmask_b32_dpp v167, v171, v175, vcc quad_perm:[2,3,0,1] row_mask:0xf bank_mask:0xf
	v_cndmask_b32_dpp v160, v156, v164, vcc quad_perm:[2,3,0,1] row_mask:0xf bank_mask:0xf
	v_cndmask_b32_dpp v168, v172, v176, vcc quad_perm:[2,3,0,1] row_mask:0xf bank_mask:0xf
	v_cndmask_b32_dpp v161, v157, v165, vcc quad_perm:[2,3,0,1] row_mask:0xf bank_mask:0xf
	v_cndmask_b32_dpp v169, v173, v177, vcc quad_perm:[2,3,0,1] row_mask:0xf bank_mask:0xf
	s_mov_b32 vcc_lo, 0x33333333
	s_mov_b32 vcc_hi, 0x33333333
	s_nop 1
	v_cndmask_b32_dpp v154, v162, v154, vcc quad_perm:[2,3,0,1] row_mask:0xf bank_mask:0xf
	v_cndmask_b32_dpp v170, v174, v170, vcc quad_perm:[2,3,0,1] row_mask:0xf bank_mask:0xf
	v_cndmask_b32_dpp v155, v163, v155, vcc quad_perm:[2,3,0,1] row_mask:0xf bank_mask:0xf
	v_cndmask_b32_dpp v171, v175, v171, vcc quad_perm:[2,3,0,1] row_mask:0xf bank_mask:0xf
	v_cndmask_b32_dpp v156, v164, v156, vcc quad_perm:[2,3,0,1] row_mask:0xf bank_mask:0xf
	v_cndmask_b32_dpp v172, v176, v172, vcc quad_perm:[2,3,0,1] row_mask:0xf bank_mask:0xf
	v_cndmask_b32_dpp v157, v165, v157, vcc quad_perm:[2,3,0,1] row_mask:0xf bank_mask:0xf
	v_cndmask_b32_dpp v173, v177, v173, vcc quad_perm:[2,3,0,1] row_mask:0xf bank_mask:0xf
	global_store_dwordx4 v179, v[154:157], s[82:83] nt
	global_store_dwordx4 v180, v[170:173], s[82:83] nt
	global_store_dwordx4 v181, v[158:161], s[82:83] nt
	global_store_dwordx4 v190, v[166:169], s[82:83] nt
	v_readlane_b32 s2, v239, 0
	s_lshr_b32 s2, s2, 6
	s_add_i32 s2, s2, 13
	s_cmp_gt_u32 s2, 20
	s_cbranch_scc1 .Lhw_seam0_done
	s_add_i32 s2, s2, 0
	s_mul_i32 s2, s2, s74
	v_readlane_b32 s9, v239, 23
	s_lshr_b32 s9, s9, 3
	s_add_i32 s2, s2, s9
	s_cmp_gt_u32 s2, 24575
	s_cbranch_scc1 .Lhw_seam0_done
	v_mbcnt_lo_u32_b32 v178, -1, 0
	v_mbcnt_hi_u32_b32 v178, -1, v178
	v_and_b32_e32 v179, 60, v178
	v_lshlrev_b32_e32 v179, 10, v179
	v_and_b32_e32 v180, 3, v178
	v_lshl_or_b32 v179, v180, 4, v179
	v_add_u32_e32 v180, 0x400, v179
	v_add_u32_e32 v181, 0x800, v179
	v_add_u32_e32 v190, 0xc00, v179
	v_lshlrev_b32_e32 v178, 2, v178
	s_cmp_lt_u32 s2, 16384
	s_cbranch_scc0 .Lhw_dn_s0_2
	s_lshr_b32 s9, s2, 9
	s_bfe_u32 s32, s2, 0x40005
	s_and_b32 s53, s2, 31
	s_lshl_b32 s69, s9, 23
	s_lshl_b32 s100, s32, 19
	s_add_i32 s69, s69, s100
	s_lshl_b32 s100, s53, 8
	s_add_i32 s69, s69, s100
	s_lshl_b32 s98, s9, 11
	s_bfe_u32 s100, s53, 0x30001
	s_lshl_b32 s100, s100, 8
	s_add_i32 s98, s98, s100
	s_lshr_b32 s100, s53, 4
	s_lshl_b32 s100, s100, 7
	s_add_i32 s98, s98, s100
	s_and_b32 s100, s53, 1
	s_lshl_b32 s100, s100, 6
	s_add_i32 s98, s98, s100
	s_lshl_b32 s98, s98, 10
	s_lshl_b32 s100, s32, 6
	s_add_i32 s98, s98, s100
	s_add_i32 s98, s98, 0x2000000
	v_readlane_b32 s82, v239, 11
	v_readlane_b32 s83, v239, 12
	s_movk_i32 s89, 8192
	s_branch .Lhw_go_s0_2

.Lhw_seam1:
	s_mov_b64 exec, -1
	v_readlane_b32 s2, v239, 0
	s_lshr_b32 s2, s2, 6
	s_add_i32 s2, s2, -1
	s_cmp_gt_u32 s2, 20
	s_cbranch_scc1 .Lhw_seam1_done
	s_add_i32 s2, s2, 21
	s_mul_i32 s2, s2, s74
	v_readlane_b32 s9, v239, 23
	s_lshr_b32 s9, s9, 3
	s_add_i32 s2, s2, s9
	s_cmp_gt_u32 s2, 24575
	s_cbranch_scc1 .Lhw_seam1_done
	v_mbcnt_lo_u32_b32 v178, -1, 0
	v_mbcnt_hi_u32_b32 v178, -1, v178
	v_and_b32_e32 v179, 60, v178
	v_lshlrev_b32_e32 v179, 10, v179
	v_and_b32_e32 v180, 3, v178
	v_lshl_or_b32 v179, v180, 4, v179
	v_add_u32_e32 v180, 0x400, v179
	v_add_u32_e32 v181, 0x800, v179
	v_add_u32_e32 v190, 0xc00, v179
	v_lshlrev_b32_e32 v178, 2, v178
	s_cmp_lt_u32 s2, 16384
	s_cbranch_scc0 .Lhw_dn_s1_0
	s_lshr_b32 s9, s2, 9
	s_bfe_u32 s32, s2, 0x40005
	s_and_b32 s53, s2, 31
	s_lshl_b32 s69, s9, 23
	s_lshl_b32 s100, s32, 19
	s_add_i32 s69, s69, s100
	s_lshl_b32 s100, s53, 8
	s_add_i32 s69, s69, s100
	s_lshl_b32 s98, s9, 11
	s_bfe_u32 s100, s53, 0x30001
	s_lshl_b32 s100, s100, 8
	s_add_i32 s98, s98, s100
	s_lshr_b32 s100, s53, 4
	s_lshl_b32 s100, s100, 7
	s_add_i32 s98, s98, s100
	s_and_b32 s100, s53, 1
	s_lshl_b32 s100, s100, 6
	s_add_i32 s98, s98, s100
	s_lshl_b32 s98, s98, 10
	s_lshl_b32 s100, s32, 6
	s_add_i32 s98, s98, s100
	s_add_i32 s98, s98, 0x2000000
	v_readlane_b32 s82, v239, 11
	v_readlane_b32 s83, v239, 12
	s_movk_i32 s89, 8192
	s_branch .Lhw_go_s1_0

.Lhw_go_s1_0:
	s_add_u32 s100, s82, s69
	s_addc_u32 s101, s83, 0
	v_readlane_b32 s82, v239, 44
	v_readlane_b32 s83, v239, 45
	s_add_u32 s82, s82, s98
	s_addc_u32 s83, s83, 0
	global_load_dword v34, v178, s[100:101] nt
	s_add_u32 s100, s100, s89
	s_addc_u32 s101, s101, 0
	global_load_dword v35, v178, s[100:101] nt
	s_add_u32 s100, s100, s89
	s_addc_u32 s101, s101, 0
	global_load_dword v36, v178, s[100:101] nt
	s_add_u32 s100, s100, s89
	s_addc_u32 s101, s101, 0
	global_load_dword v37, v178, s[100:101] nt
	s_add_u32 s100, s100, s89
	s_addc_u32 s101, s101, 0
	global_load_dword v38, v178, s[100:101] nt
	s_add_u32 s100, s100, s89
	s_addc_u32 s101, s101, 0
	global_load_dword v39, v178, s[100:101] nt
	s_add_u32 s100, s100, s89
	s_addc_u32 s101, s101, 0
	global_load_dword v40, v178, s[100:101] nt
	s_add_u32 s100, s100, s89
	s_addc_u32 s101, s101, 0
	global_load_dword v41, v178, s[100:101] nt
	s_add_u32 s100, s100, s89
	s_addc_u32 s101, s101, 0
	global_load_dword v42, v178, s[100:101] nt
	s_add_u32 s100, s100, s89
	s_addc_u32 s101, s101, 0
	global_load_dword v43, v178, s[100:101] nt
	s_add_u32 s100, s100, s89
	s_addc_u32 s101, s101, 0
	global_load_dword v44, v178, s[100:101] nt
	s_add_u32 s100, s100, s89
	s_addc_u32 s101, s101, 0
	global_load_dword v45, v178, s[100:101] nt
	s_add_u32 s100, s100, s89
	s_addc_u32 s101, s101, 0
	global_load_dword v46, v178, s[100:101] nt
	s_add_u32 s100, s100, s89
	s_addc_u32 s101, s101, 0
	global_load_dword v47, v178, s[100:101] nt
	s_add_u32 s100, s100, s89
	s_addc_u32 s101, s101, 0
	global_load_dword v48, v178, s[100:101] nt
	s_add_u32 s100, s100, s89
	s_addc_u32 s101, s101, 0
	global_load_dword v49, v178, s[100:101] nt
	s_add_u32 s100, s100, s89
	s_addc_u32 s101, s101, 0
	global_load_dword v50, v178, s[100:101] nt
	s_add_u32 s100, s100, s89
	s_addc_u32 s101, s101, 0
	global_load_dword v51, v178, s[100:101] nt
	s_add_u32 s100, s100, s89
	s_addc_u32 s101, s101, 0
	global_load_dword v52, v178, s[100:101] nt
	s_add_u32 s100, s100, s89
	s_addc_u32 s101, s101, 0
	global_load_dword v53, v178, s[100:101] nt
	s_add_u32 s100, s100, s89
	s_addc_u32 s101, s101, 0
	global_load_dword v54, v178, s[100:101] nt
	s_add_u32 s100, s100, s89
	s_addc_u32 s101, s101, 0
	global_load_dword v55, v178, s[100:101] nt
	s_add_u32 s100, s100, s89
	s_addc_u32 s101, s101, 0
	global_load_dword v56, v178, s[100:101] nt
	s_add_u32 s100, s100, s89
	s_addc_u32 s101, s101, 0
	global_load_dword v57, v178, s[100:101] nt
	s_add_u32 s100, s100, s89
	s_addc_u32 s101, s101, 0
	global_load_dword v58, v178, s[100:101] nt
	s_add_u32 s100, s100, s89
	s_addc_u32 s101, s101, 0
	global_load_dword v59, v178, s[100:101] nt
	s_add_u32 s100, s100, s89
	s_addc_u32 s101, s101, 0
	global_load_dword v60, v178, s[100:101] nt
	s_add_u32 s100, s100, s89
	s_addc_u32 s101, s101, 0
	global_load_dword v61, v178, s[100:101] nt
	s_add_u32 s100, s100, s89
	s_addc_u32 s101, s101, 0
	global_load_dword v62, v178, s[100:101] nt
	s_add_u32 s100, s100, s89
	s_addc_u32 s101, s101, 0
	global_load_dword v63, v178, s[100:101] nt
	s_add_u32 s100, s100, s89
	s_addc_u32 s101, s101, 0
	global_load_dword v64, v178, s[100:101] nt
	s_add_u32 s100, s100, s89
	s_addc_u32 s101, s101, 0
	global_load_dword v65, v178, s[100:101] nt
	s_add_u32 s100, s100, s89
	s_addc_u32 s101, s101, 0
	global_load_dword v66, v178, s[100:101] nt
	s_add_u32 s100, s100, s89
	s_addc_u32 s101, s101, 0
	global_load_dword v67, v178, s[100:101] nt
	s_add_u32 s100, s100, s89
	s_addc_u32 s101, s101, 0
	global_load_dword v68, v178, s[100:101] nt
	s_add_u32 s100, s100, s89
	s_addc_u32 s101, s101, 0
	global_load_dword v69, v178, s[100:101] nt
	s_add_u32 s100, s100, s89
	s_addc_u32 s101, s101, 0
	global_load_dword v70, v178, s[100:101] nt
	s_add_u32 s100, s100, s89
	s_addc_u32 s101, s101, 0
	global_load_dword v71, v178, s[100:101] nt
	s_add_u32 s100, s100, s89
	s_addc_u32 s101, s101, 0
	global_load_dword v72, v178, s[100:101] nt
	s_add_u32 s100, s100, s89
	s_addc_u32 s101, s101, 0
	global_load_dword v73, v178, s[100:101] nt
	s_add_u32 s100, s100, s89
	s_addc_u32 s101, s101, 0
	global_load_dword v74, v178, s[100:101] nt
	s_add_u32 s100, s100, s89
	s_addc_u32 s101, s101, 0
	global_load_dword v75, v178, s[100:101] nt
	s_add_u32 s100, s100, s89
	s_addc_u32 s101, s101, 0
	global_load_dword v76, v178, s[100:101] nt
	s_add_u32 s100, s100, s89
	s_addc_u32 s101, s101, 0
	global_load_dword v77, v178, s[100:101] nt
	s_add_u32 s100, s100, s89
	s_addc_u32 s101, s101, 0
	global_load_dword v78, v178, s[100:101] nt
	s_add_u32 s100, s100, s89
	s_addc_u32 s101, s101, 0
	global_load_dword v79, v178, s[100:101] nt
	s_add_u32 s100, s100, s89
	s_addc_u32 s101, s101, 0
	global_load_dword v80, v178, s[100:101] nt
	s_add_u32 s100, s100, s89
	s_addc_u32 s101, s101, 0
	global_load_dword v81, v178, s[100:101] nt
	s_add_u32 s100, s100, s89
	s_addc_u32 s101, s101, 0
	global_load_dword v82, v178, s[100:101] nt
	s_add_u32 s100, s100, s89
	s_addc_u32 s101, s101, 0
	global_load_dword v83, v178, s[100:101] nt
	s_add_u32 s100, s100, s89
	s_addc_u32 s101, s101, 0
	global_load_dword v84, v178, s[100:101] nt
	s_add_u32 s100, s100, s89
	s_addc_u32 s101, s101, 0
	global_load_dword v85, v178, s[100:101] nt
	s_add_u32 s100, s100, s89
	s_addc_u32 s101, s101, 0
	global_load_dword v86, v178, s[100:101] nt
	s_add_u32 s100, s100, s89
	s_addc_u32 s101, s101, 0
	global_load_dword v87, v178, s[100:101] nt
	s_add_u32 s100, s100, s89
	s_addc_u32 s101, s101, 0
	global_load_dword v88, v178, s[100:101] nt
	s_add_u32 s100, s100, s89
	s_addc_u32 s101, s101, 0
	global_load_dword v89, v178, s[100:101] nt
	s_add_u32 s100, s100, s89
	s_addc_u32 s101, s101, 0
	global_load_dword v90, v178, s[100:101] nt
	s_add_u32 s100, s100, s89
	s_addc_u32 s101, s101, 0
	global_load_dword v91, v178, s[100:101] nt
	s_add_u32 s100, s100, s89
	s_addc_u32 s101, s101, 0
	global_load_dword v92, v178, s[100:101] nt
	s_add_u32 s100, s100, s89
	s_addc_u32 s101, s101, 0
	global_load_dword v93, v178, s[100:101] nt
	s_add_u32 s100, s100, s89
	s_addc_u32 s101, s101, 0
	global_load_dword v94, v178, s[100:101] nt
	s_add_u32 s100, s100, s89
	s_addc_u32 s101, s101, 0
	global_load_dword v95, v178, s[100:101] nt
	s_add_u32 s100, s100, s89
	s_addc_u32 s101, s101, 0
	global_load_dword v96, v178, s[100:101] nt
	s_add_u32 s100, s100, s89
	s_addc_u32 s101, s101, 0
	global_load_dword v97, v178, s[100:101] nt
	s_add_u32 s100, s100, s89
	s_addc_u32 s101, s101, 0
	s_waitcnt vmcnt(48)
	v_mul_f32_e32 v34, 0x42000000, v34
	v_mul_f32_e32 v35, 0x42000000, v35
	v_mul_f32_e32 v36, 0x42000000, v36
	v_mul_f32_e32 v37, 0x42000000, v37
	v_mul_f32_e32 v38, 0x42000000, v38
	v_mul_f32_e32 v39, 0x42000000, v39
	v_mul_f32_e32 v40, 0x42000000, v40
	v_mul_f32_e32 v41, 0x42000000, v41
	v_mul_f32_e32 v42, 0x42000000, v42
	v_mul_f32_e32 v43, 0x42000000, v43
	v_mul_f32_e32 v44, 0x42000000, v44
	v_mul_f32_e32 v45, 0x42000000, v45
	v_mul_f32_e32 v46, 0x42000000, v46
	v_mul_f32_e32 v47, 0x42000000, v47
	v_mul_f32_e32 v48, 0x42000000, v48
	v_mul_f32_e32 v49, 0x42000000, v49
	v_cvt_pk_fp8_f32 v154, v34, v35
	v_cvt_pk_fp8_f32 v155, v38, v39
	v_cvt_pk_fp8_f32 v156, v42, v43
	v_cvt_pk_fp8_f32 v157, v46, v47
	v_cvt_pk_fp8_f32 v154, v36, v37 op_sel:[0,0,1]
	v_cvt_pk_fp8_f32 v155, v40, v41 op_sel:[0,0,1]
	v_cvt_pk_fp8_f32 v156, v44, v45 op_sel:[0,0,1]
	v_cvt_pk_fp8_f32 v157, v48, v49 op_sel:[0,0,1]
	s_waitcnt vmcnt(32)
	v_mul_f32_e32 v50, 0x42000000, v50
	v_mul_f32_e32 v51, 0x42000000, v51
	v_mul_f32_e32 v52, 0x42000000, v52
	v_mul_f32_e32 v53, 0x42000000, v53
	v_mul_f32_e32 v54, 0x42000000, v54
	v_mul_f32_e32 v55, 0x42000000, v55
	v_mul_f32_e32 v56, 0x42000000, v56
	v_mul_f32_e32 v57, 0x42000000, v57
	v_mul_f32_e32 v58, 0x42000000, v58
	v_mul_f32_e32 v59, 0x42000000, v59
	v_mul_f32_e32 v60, 0x42000000, v60
	v_mul_f32_e32 v61, 0x42000000, v61
	v_mul_f32_e32 v62, 0x42000000, v62
	v_mul_f32_e32 v63, 0x42000000, v63
	v_mul_f32_e32 v64, 0x42000000, v64
	v_mul_f32_e32 v65, 0x42000000, v65
	v_cvt_pk_fp8_f32 v158, v50, v51
	v_cvt_pk_fp8_f32 v159, v54, v55
	v_cvt_pk_fp8_f32 v160, v58, v59
	v_cvt_pk_fp8_f32 v161, v62, v63
	v_cvt_pk_fp8_f32 v158, v52, v53 op_sel:[0,0,1]
	v_cvt_pk_fp8_f32 v159, v56, v57 op_sel:[0,0,1]
	v_cvt_pk_fp8_f32 v160, v60, v61 op_sel:[0,0,1]
	v_cvt_pk_fp8_f32 v161, v64, v65 op_sel:[0,0,1]
	s_waitcnt vmcnt(16)
	v_mul_f32_e32 v66, 0x42000000, v66
	v_mul_f32_e32 v67, 0x42000000, v67
	v_mul_f32_e32 v68, 0x42000000, v68
	v_mul_f32_e32 v69, 0x42000000, v69
	v_mul_f32_e32 v70, 0x42000000, v70
	v_mul_f32_e32 v71, 0x42000000, v71
	v_mul_f32_e32 v72, 0x42000000, v72
	v_mul_f32_e32 v73, 0x42000000, v73
	v_mul_f32_e32 v74, 0x42000000, v74
	v_mul_f32_e32 v75, 0x42000000, v75
	v_mul_f32_e32 v76, 0x42000000, v76
	v_mul_f32_e32 v77, 0x42000000, v77
	v_mul_f32_e32 v78, 0x42000000, v78
	v_mul_f32_e32 v79, 0x42000000, v79
	v_mul_f32_e32 v80, 0x42000000, v80
	v_mul_f32_e32 v81, 0x42000000, v81
	v_cvt_pk_fp8_f32 v162, v66, v67
	v_cvt_pk_fp8_f32 v163, v70, v71
	v_cvt_pk_fp8_f32 v164, v74, v75
	v_cvt_pk_fp8_f32 v165, v78, v79
	v_cvt_pk_fp8_f32 v162, v68, v69 op_sel:[0,0,1]
	v_cvt_pk_fp8_f32 v163, v72, v73 op_sel:[0,0,1]
	v_cvt_pk_fp8_f32 v164, v76, v77 op_sel:[0,0,1]
	v_cvt_pk_fp8_f32 v165, v80, v81 op_sel:[0,0,1]
	s_waitcnt vmcnt(0)
	v_mul_f32_e32 v82, 0x42000000, v82
	v_mul_f32_e32 v83, 0x42000000, v83
	v_mul_f32_e32 v84, 0x42000000, v84
	v_mul_f32_e32 v85, 0x42000000, v85
	v_mul_f32_e32 v86, 0x42000000, v86
	v_mul_f32_e32 v87, 0x42000000, v87
	v_mul_f32_e32 v88, 0x42000000, v88
	v_mul_f32_e32 v89, 0x42000000, v89
	v_mul_f32_e32 v90, 0x42000000, v90
	v_mul_f32_e32 v91, 0x42000000, v91
	v_mul_f32_e32 v92, 0x42000000, v92
	v_mul_f32_e32 v93, 0x42000000, v93
	v_mul_f32_e32 v94, 0x42000000, v94
	v_mul_f32_e32 v95, 0x42000000, v95
	v_mul_f32_e32 v96, 0x42000000, v96
	v_mul_f32_e32 v97, 0x42000000, v97
	v_cvt_pk_fp8_f32 v166, v82, v83
	v_cvt_pk_fp8_f32 v167, v86, v87
	v_cvt_pk_fp8_f32 v168, v90, v91
	v_cvt_pk_fp8_f32 v169, v94, v95
	v_cvt_pk_fp8_f32 v166, v84, v85 op_sel:[0,0,1]
	v_cvt_pk_fp8_f32 v167, v88, v89 op_sel:[0,0,1]
	v_cvt_pk_fp8_f32 v168, v92, v93 op_sel:[0,0,1]
	v_cvt_pk_fp8_f32 v169, v96, v97 op_sel:[0,0,1]
	s_mov_b32 vcc_lo, 0xaaaaaaaa
	s_mov_b32 vcc_hi, 0xaaaaaaaa
	s_nop 1
	v_cndmask_b32_dpp v170, v154, v158, vcc quad_perm:[1,0,3,2] row_mask:0xf bank_mask:0xf
	v_cndmask_b32_dpp v174, v162, v166, vcc quad_perm:[1,0,3,2] row_mask:0xf bank_mask:0xf
	v_cndmask_b32_dpp v171, v155, v159, vcc quad_perm:[1,0,3,2] row_mask:0xf bank_mask:0xf
	v_cndmask_b32_dpp v175, v163, v167, vcc quad_perm:[1,0,3,2] row_mask:0xf bank_mask:0xf
	v_cndmask_b32_dpp v172, v156, v160, vcc quad_perm:[1,0,3,2] row_mask:0xf bank_mask:0xf
	v_cndmask_b32_dpp v176, v164, v168, vcc quad_perm:[1,0,3,2] row_mask:0xf bank_mask:0xf
	v_cndmask_b32_dpp v173, v157, v161, vcc quad_perm:[1,0,3,2] row_mask:0xf bank_mask:0xf
	v_cndmask_b32_dpp v177, v165, v169, vcc quad_perm:[1,0,3,2] row_mask:0xf bank_mask:0xf
	s_mov_b32 vcc_lo, 0x55555555
	s_mov_b32 vcc_hi, 0x55555555
	s_nop 1
	v_cndmask_b32_dpp v154, v158, v154, vcc quad_perm:[1,0,3,2] row_mask:0xf bank_mask:0xf
	v_cndmask_b32_dpp v162, v166, v162, vcc quad_perm:[1,0,3,2] row_mask:0xf bank_mask:0xf
	v_cndmask_b32_dpp v155, v159, v155, vcc quad_perm:[1,0,3,2] row_mask:0xf bank_mask:0xf
	v_cndmask_b32_dpp v163, v167, v163, vcc quad_perm:[1,0,3,2] row_mask:0xf bank_mask:0xf
	v_cndmask_b32_dpp v156, v160, v156, vcc quad_perm:[1,0,3,2] row_mask:0xf bank_mask:0xf
	v_cndmask_b32_dpp v164, v168, v164, vcc quad_perm:[1,0,3,2] row_mask:0xf bank_mask:0xf
	v_cndmask_b32_dpp v157, v161, v157, vcc quad_perm:[1,0,3,2] row_mask:0xf bank_mask:0xf
	v_cndmask_b32_dpp v165, v169, v165, vcc quad_perm:[1,0,3,2] row_mask:0xf bank_mask:0xf
	s_mov_b32 vcc_lo, 0xcccccccc
	s_mov_b32 vcc_hi, 0xcccccccc
	s_nop 1
	v_cndmask_b32_dpp v158, v154, v162, vcc quad_perm:[2,3,0,1] row_mask:0xf bank_mask:0xf
	v_cndmask_b32_dpp v166, v170, v174, vcc quad_perm:[2,3,0,1] row_mask:0xf bank_mask:0xf
	v_cndmask_b32_dpp v159, v155, v163, vcc quad_perm:[2,3,0,1] row_mask:0xf bank_mask:0xf
	v_cndmask_b32_dpp v167, v171, v175, vcc quad_perm:[2,3,0,1] row_mask:0xf bank_mask:0xf
	v_cndmask_b32_dpp v160, v156, v164, vcc quad_perm:[2,3,0,1] row_mask:0xf bank_mask:0xf
	v_cndmask_b32_dpp v168, v172, v176, vcc quad_perm:[2,3,0,1] row_mask:0xf bank_mask:0xf
	v_cndmask_b32_dpp v161, v157, v165, vcc quad_perm:[2,3,0,1] row_mask:0xf bank_mask:0xf
	v_cndmask_b32_dpp v169, v173, v177, vcc quad_perm:[2,3,0,1] row_mask:0xf bank_mask:0xf
	s_mov_b32 vcc_lo, 0x33333333
	s_mov_b32 vcc_hi, 0x33333333
	s_nop 1
	v_cndmask_b32_dpp v154, v162, v154, vcc quad_perm:[2,3,0,1] row_mask:0xf bank_mask:0xf
	v_cndmask_b32_dpp v170, v174, v170, vcc quad_perm:[2,3,0,1] row_mask:0xf bank_mask:0xf
	v_cndmask_b32_dpp v155, v163, v155, vcc quad_perm:[2,3,0,1] row_mask:0xf bank_mask:0xf
	v_cndmask_b32_dpp v171, v175, v171, vcc quad_perm:[2,3,0,1] row_mask:0xf bank_mask:0xf
	v_cndmask_b32_dpp v156, v164, v156, vcc quad_perm:[2,3,0,1] row_mask:0xf bank_mask:0xf
	v_cndmask_b32_dpp v172, v176, v172, vcc quad_perm:[2,3,0,1] row_mask:0xf bank_mask:0xf
	v_cndmask_b32_dpp v157, v165, v157, vcc quad_perm:[2,3,0,1] row_mask:0xf bank_mask:0xf
	v_cndmask_b32_dpp v173, v177, v173, vcc quad_perm:[2,3,0,1] row_mask:0xf bank_mask:0xf
	global_store_dwordx4 v179, v[154:157], s[82:83] nt
	global_store_dwordx4 v180, v[170:173], s[82:83] nt
	global_store_dwordx4 v181, v[158:161], s[82:83] nt
	global_store_dwordx4 v190, v[166:169], s[82:83] nt
	v_readlane_b32 s2, v239, 0
	s_lshr_b32 s2, s2, 6
	s_add_i32 s2, s2, 6
	s_cmp_gt_u32 s2, 20
	s_cbranch_scc1 .Lhw_seam1_done
	s_add_i32 s2, s2, 21
	s_mul_i32 s2, s2, s74
	v_readlane_b32 s9, v239, 23
	s_lshr_b32 s9, s9, 3
	s_add_i32 s2, s2, s9
	s_cmp_gt_u32 s2, 24575
	s_cbranch_scc1 .Lhw_seam1_done
	v_mbcnt_lo_u32_b32 v178, -1, 0
	v_mbcnt_hi_u32_b32 v178, -1, v178
	v_and_b32_e32 v179, 60, v178
	v_lshlrev_b32_e32 v179, 10, v179
	v_and_b32_e32 v180, 3, v178
	v_lshl_or_b32 v179, v180, 4, v179
	v_add_u32_e32 v180, 0x400, v179
	v_add_u32_e32 v181, 0x800, v179
	v_add_u32_e32 v190, 0xc00, v179
	v_lshlrev_b32_e32 v178, 2, v178
	s_cmp_lt_u32 s2, 16384
	s_cbranch_scc0 .Lhw_dn_s1_1
	s_lshr_b32 s9, s2, 9
	s_bfe_u32 s32, s2, 0x40005
	s_and_b32 s53, s2, 31
	s_lshl_b32 s69, s9, 23
	s_lshl_b32 s100, s32, 19
	s_add_i32 s69, s69, s100
	s_lshl_b32 s100, s53, 8
	s_add_i32 s69, s69, s100
	s_lshl_b32 s98, s9, 11
	s_bfe_u32 s100, s53, 0x30001
	s_lshl_b32 s100, s100, 8
	s_add_i32 s98, s98, s100
	s_lshr_b32 s100, s53, 4
	s_lshl_b32 s100, s100, 7
	s_add_i32 s98, s98, s100
	s_and_b32 s100, s53, 1
	s_lshl_b32 s100, s100, 6
	s_add_i32 s98, s98, s100
	s_lshl_b32 s98, s98, 10
	s_lshl_b32 s100, s32, 6
	s_add_i32 s98, s98, s100
	s_add_i32 s98, s98, 0x2000000
	v_readlane_b32 s82, v239, 11
	v_readlane_b32 s83, v239, 12
	s_movk_i32 s89, 8192
	s_branch .Lhw_go_s1_1

.Lhw_go_s1_1:
	s_add_u32 s100, s82, s69
	s_addc_u32 s101, s83, 0
	v_readlane_b32 s82, v239, 44
	v_readlane_b32 s83, v239, 45
	s_add_u32 s82, s82, s98
	s_addc_u32 s83, s83, 0
	global_load_dword v34, v178, s[100:101] nt
	s_add_u32 s100, s100, s89
	s_addc_u32 s101, s101, 0
	global_load_dword v35, v178, s[100:101] nt
	s_add_u32 s100, s100, s89
	s_addc_u32 s101, s101, 0
	global_load_dword v36, v178, s[100:101] nt
	s_add_u32 s100, s100, s89
	s_addc_u32 s101, s101, 0
	global_load_dword v37, v178, s[100:101] nt
	s_add_u32 s100, s100, s89
	s_addc_u32 s101, s101, 0
	global_load_dword v38, v178, s[100:101] nt
	s_add_u32 s100, s100, s89
	s_addc_u32 s101, s101, 0
	global_load_dword v39, v178, s[100:101] nt
	s_add_u32 s100, s100, s89
	s_addc_u32 s101, s101, 0
	global_load_dword v40, v178, s[100:101] nt
	s_add_u32 s100, s100, s89
	s_addc_u32 s101, s101, 0
	global_load_dword v41, v178, s[100:101] nt
	s_add_u32 s100, s100, s89
	s_addc_u32 s101, s101, 0
	global_load_dword v42, v178, s[100:101] nt
	s_add_u32 s100, s100, s89
	s_addc_u32 s101, s101, 0
	global_load_dword v43, v178, s[100:101] nt
	s_add_u32 s100, s100, s89
	s_addc_u32 s101, s101, 0
	global_load_dword v44, v178, s[100:101] nt
	s_add_u32 s100, s100, s89
	s_addc_u32 s101, s101, 0
	global_load_dword v45, v178, s[100:101] nt
	s_add_u32 s100, s100, s89
	s_addc_u32 s101, s101, 0
	global_load_dword v46, v178, s[100:101] nt
	s_add_u32 s100, s100, s89
	s_addc_u32 s101, s101, 0
	global_load_dword v47, v178, s[100:101] nt
	s_add_u32 s100, s100, s89
	s_addc_u32 s101, s101, 0
	global_load_dword v48, v178, s[100:101] nt
	s_add_u32 s100, s100, s89
	s_addc_u32 s101, s101, 0
	global_load_dword v49, v178, s[100:101] nt
	s_add_u32 s100, s100, s89
	s_addc_u32 s101, s101, 0
	global_load_dword v50, v178, s[100:101] nt
	s_add_u32 s100, s100, s89
	s_addc_u32 s101, s101, 0
	global_load_dword v51, v178, s[100:101] nt
	s_add_u32 s100, s100, s89
	s_addc_u32 s101, s101, 0
	global_load_dword v52, v178, s[100:101] nt
	s_add_u32 s100, s100, s89
	s_addc_u32 s101, s101, 0
	global_load_dword v53, v178, s[100:101] nt
	s_add_u32 s100, s100, s89
	s_addc_u32 s101, s101, 0
	global_load_dword v54, v178, s[100:101] nt
	s_add_u32 s100, s100, s89
	s_addc_u32 s101, s101, 0
	global_load_dword v55, v178, s[100:101] nt
	s_add_u32 s100, s100, s89
	s_addc_u32 s101, s101, 0
	global_load_dword v56, v178, s[100:101] nt
	s_add_u32 s100, s100, s89
	s_addc_u32 s101, s101, 0
	global_load_dword v57, v178, s[100:101] nt
	s_add_u32 s100, s100, s89
	s_addc_u32 s101, s101, 0
	global_load_dword v58, v178, s[100:101] nt
	s_add_u32 s100, s100, s89
	s_addc_u32 s101, s101, 0
	global_load_dword v59, v178, s[100:101] nt
	s_add_u32 s100, s100, s89
	s_addc_u32 s101, s101, 0
	global_load_dword v60, v178, s[100:101] nt
	s_add_u32 s100, s100, s89
	s_addc_u32 s101, s101, 0
	global_load_dword v61, v178, s[100:101] nt
	s_add_u32 s100, s100, s89
	s_addc_u32 s101, s101, 0
	global_load_dword v62, v178, s[100:101] nt
	s_add_u32 s100, s100, s89
	s_addc_u32 s101, s101, 0
	global_load_dword v63, v178, s[100:101] nt
	s_add_u32 s100, s100, s89
	s_addc_u32 s101, s101, 0
	global_load_dword v64, v178, s[100:101] nt
	s_add_u32 s100, s100, s89
	s_addc_u32 s101, s101, 0
	global_load_dword v65, v178, s[100:101] nt
	s_add_u32 s100, s100, s89
	s_addc_u32 s101, s101, 0
	global_load_dword v66, v178, s[100:101] nt
	s_add_u32 s100, s100, s89
	s_addc_u32 s101, s101, 0
	global_load_dword v67, v178, s[100:101] nt
	s_add_u32 s100, s100, s89
	s_addc_u32 s101, s101, 0
	global_load_dword v68, v178, s[100:101] nt
	s_add_u32 s100, s100, s89
	s_addc_u32 s101, s101, 0
	global_load_dword v69, v178, s[100:101] nt
	s_add_u32 s100, s100, s89
	s_addc_u32 s101, s101, 0
	global_load_dword v70, v178, s[100:101] nt
	s_add_u32 s100, s100, s89
	s_addc_u32 s101, s101, 0
	global_load_dword v71, v178, s[100:101] nt
	s_add_u32 s100, s100, s89
	s_addc_u32 s101, s101, 0
	global_load_dword v72, v178, s[100:101] nt
	s_add_u32 s100, s100, s89
	s_addc_u32 s101, s101, 0
	global_load_dword v73, v178, s[100:101] nt
	s_add_u32 s100, s100, s89
	s_addc_u32 s101, s101, 0
	global_load_dword v74, v178, s[100:101] nt
	s_add_u32 s100, s100, s89
	s_addc_u32 s101, s101, 0
	global_load_dword v75, v178, s[100:101] nt
	s_add_u32 s100, s100, s89
	s_addc_u32 s101, s101, 0
	global_load_dword v76, v178, s[100:101] nt
	s_add_u32 s100, s100, s89
	s_addc_u32 s101, s101, 0
	global_load_dword v77, v178, s[100:101] nt
	s_add_u32 s100, s100, s89
	s_addc_u32 s101, s101, 0
	global_load_dword v78, v178, s[100:101] nt
	s_add_u32 s100, s100, s89
	s_addc_u32 s101, s101, 0
	global_load_dword v79, v178, s[100:101] nt
	s_add_u32 s100, s100, s89
	s_addc_u32 s101, s101, 0
	global_load_dword v80, v178, s[100:101] nt
	s_add_u32 s100, s100, s89
	s_addc_u32 s101, s101, 0
	global_load_dword v81, v178, s[100:101] nt
	s_add_u32 s100, s100, s89
	s_addc_u32 s101, s101, 0
	global_load_dword v82, v178, s[100:101] nt
	s_add_u32 s100, s100, s89
	s_addc_u32 s101, s101, 0
	global_load_dword v83, v178, s[100:101] nt
	s_add_u32 s100, s100, s89
	s_addc_u32 s101, s101, 0
	global_load_dword v84, v178, s[100:101] nt
	s_add_u32 s100, s100, s89
	s_addc_u32 s101, s101, 0
	global_load_dword v85, v178, s[100:101] nt
	s_add_u32 s100, s100, s89
	s_addc_u32 s101, s101, 0
	global_load_dword v86, v178, s[100:101] nt
	s_add_u32 s100, s100, s89
	s_addc_u32 s101, s101, 0
	global_load_dword v87, v178, s[100:101] nt
	s_add_u32 s100, s100, s89
	s_addc_u32 s101, s101, 0
	global_load_dword v88, v178, s[100:101] nt
	s_add_u32 s100, s100, s89
	s_addc_u32 s101, s101, 0
	global_load_dword v89, v178, s[100:101] nt
	s_add_u32 s100, s100, s89
	s_addc_u32 s101, s101, 0
	global_load_dword v90, v178, s[100:101] nt
	s_add_u32 s100, s100, s89
	s_addc_u32 s101, s101, 0
	global_load_dword v91, v178, s[100:101] nt
	s_add_u32 s100, s100, s89
	s_addc_u32 s101, s101, 0
	global_load_dword v92, v178, s[100:101] nt
	s_add_u32 s100, s100, s89
	s_addc_u32 s101, s101, 0
	global_load_dword v93, v178, s[100:101] nt
	s_add_u32 s100, s100, s89
	s_addc_u32 s101, s101, 0
	global_load_dword v94, v178, s[100:101] nt
	s_add_u32 s100, s100, s89
	s_addc_u32 s101, s101, 0
	global_load_dword v95, v178, s[100:101] nt
	s_add_u32 s100, s100, s89
	s_addc_u32 s101, s101, 0
	global_load_dword v96, v178, s[100:101] nt
	s_add_u32 s100, s100, s89
	s_addc_u32 s101, s101, 0
	global_load_dword v97, v178, s[100:101] nt
	s_add_u32 s100, s100, s89
	s_addc_u32 s101, s101, 0
	s_waitcnt vmcnt(48)
	v_mul_f32_e32 v34, 0x42000000, v34
	v_mul_f32_e32 v35, 0x42000000, v35
	v_mul_f32_e32 v36, 0x42000000, v36
	v_mul_f32_e32 v37, 0x42000000, v37
	v_mul_f32_e32 v38, 0x42000000, v38
	v_mul_f32_e32 v39, 0x42000000, v39
	v_mul_f32_e32 v40, 0x42000000, v40
	v_mul_f32_e32 v41, 0x42000000, v41
	v_mul_f32_e32 v42, 0x42000000, v42
	v_mul_f32_e32 v43, 0x42000000, v43
	v_mul_f32_e32 v44, 0x42000000, v44
	v_mul_f32_e32 v45, 0x42000000, v45
	v_mul_f32_e32 v46, 0x42000000, v46
	v_mul_f32_e32 v47, 0x42000000, v47
	v_mul_f32_e32 v48, 0x42000000, v48
	v_mul_f32_e32 v49, 0x42000000, v49
	v_cvt_pk_fp8_f32 v154, v34, v35
	v_cvt_pk_fp8_f32 v155, v38, v39
	v_cvt_pk_fp8_f32 v156, v42, v43
	v_cvt_pk_fp8_f32 v157, v46, v47
	v_cvt_pk_fp8_f32 v154, v36, v37 op_sel:[0,0,1]
	v_cvt_pk_fp8_f32 v155, v40, v41 op_sel:[0,0,1]
	v_cvt_pk_fp8_f32 v156, v44, v45 op_sel:[0,0,1]
	v_cvt_pk_fp8_f32 v157, v48, v49 op_sel:[0,0,1]
	s_waitcnt vmcnt(32)
	v_mul_f32_e32 v50, 0x42000000, v50
	v_mul_f32_e32 v51, 0x42000000, v51
	v_mul_f32_e32 v52, 0x42000000, v52
	v_mul_f32_e32 v53, 0x42000000, v53
	v_mul_f32_e32 v54, 0x42000000, v54
	v_mul_f32_e32 v55, 0x42000000, v55
	v_mul_f32_e32 v56, 0x42000000, v56
	v_mul_f32_e32 v57, 0x42000000, v57
	v_mul_f32_e32 v58, 0x42000000, v58
	v_mul_f32_e32 v59, 0x42000000, v59
	v_mul_f32_e32 v60, 0x42000000, v60
	v_mul_f32_e32 v61, 0x42000000, v61
	v_mul_f32_e32 v62, 0x42000000, v62
	v_mul_f32_e32 v63, 0x42000000, v63
	v_mul_f32_e32 v64, 0x42000000, v64
	v_mul_f32_e32 v65, 0x42000000, v65
	v_cvt_pk_fp8_f32 v158, v50, v51
	v_cvt_pk_fp8_f32 v159, v54, v55
	v_cvt_pk_fp8_f32 v160, v58, v59
	v_cvt_pk_fp8_f32 v161, v62, v63
	v_cvt_pk_fp8_f32 v158, v52, v53 op_sel:[0,0,1]
	v_cvt_pk_fp8_f32 v159, v56, v57 op_sel:[0,0,1]
	v_cvt_pk_fp8_f32 v160, v60, v61 op_sel:[0,0,1]
	v_cvt_pk_fp8_f32 v161, v64, v65 op_sel:[0,0,1]
	s_waitcnt vmcnt(16)
	v_mul_f32_e32 v66, 0x42000000, v66
	v_mul_f32_e32 v67, 0x42000000, v67
	v_mul_f32_e32 v68, 0x42000000, v68
	v_mul_f32_e32 v69, 0x42000000, v69
	v_mul_f32_e32 v70, 0x42000000, v70
	v_mul_f32_e32 v71, 0x42000000, v71
	v_mul_f32_e32 v72, 0x42000000, v72
	v_mul_f32_e32 v73, 0x42000000, v73
	v_mul_f32_e32 v74, 0x42000000, v74
	v_mul_f32_e32 v75, 0x42000000, v75
	v_mul_f32_e32 v76, 0x42000000, v76
	v_mul_f32_e32 v77, 0x42000000, v77
	v_mul_f32_e32 v78, 0x42000000, v78
	v_mul_f32_e32 v79, 0x42000000, v79
	v_mul_f32_e32 v80, 0x42000000, v80
	v_mul_f32_e32 v81, 0x42000000, v81
	v_cvt_pk_fp8_f32 v162, v66, v67
	v_cvt_pk_fp8_f32 v163, v70, v71
	v_cvt_pk_fp8_f32 v164, v74, v75
	v_cvt_pk_fp8_f32 v165, v78, v79
	v_cvt_pk_fp8_f32 v162, v68, v69 op_sel:[0,0,1]
	v_cvt_pk_fp8_f32 v163, v72, v73 op_sel:[0,0,1]
	v_cvt_pk_fp8_f32 v164, v76, v77 op_sel:[0,0,1]
	v_cvt_pk_fp8_f32 v165, v80, v81 op_sel:[0,0,1]
	s_waitcnt vmcnt(0)
	v_mul_f32_e32 v82, 0x42000000, v82
	v_mul_f32_e32 v83, 0x42000000, v83
	v_mul_f32_e32 v84, 0x42000000, v84
	v_mul_f32_e32 v85, 0x42000000, v85
	v_mul_f32_e32 v86, 0x42000000, v86
	v_mul_f32_e32 v87, 0x42000000, v87
	v_mul_f32_e32 v88, 0x42000000, v88
	v_mul_f32_e32 v89, 0x42000000, v89
	v_mul_f32_e32 v90, 0x42000000, v90
	v_mul_f32_e32 v91, 0x42000000, v91
	v_mul_f32_e32 v92, 0x42000000, v92
	v_mul_f32_e32 v93, 0x42000000, v93
	v_mul_f32_e32 v94, 0x42000000, v94
	v_mul_f32_e32 v95, 0x42000000, v95
	v_mul_f32_e32 v96, 0x42000000, v96
	v_mul_f32_e32 v97, 0x42000000, v97
	v_cvt_pk_fp8_f32 v166, v82, v83
	v_cvt_pk_fp8_f32 v167, v86, v87
	v_cvt_pk_fp8_f32 v168, v90, v91
	v_cvt_pk_fp8_f32 v169, v94, v95
	v_cvt_pk_fp8_f32 v166, v84, v85 op_sel:[0,0,1]
	v_cvt_pk_fp8_f32 v167, v88, v89 op_sel:[0,0,1]
	v_cvt_pk_fp8_f32 v168, v92, v93 op_sel:[0,0,1]
	v_cvt_pk_fp8_f32 v169, v96, v97 op_sel:[0,0,1]
	s_mov_b32 vcc_lo, 0xaaaaaaaa
	s_mov_b32 vcc_hi, 0xaaaaaaaa
	s_nop 1
	v_cndmask_b32_dpp v170, v154, v158, vcc quad_perm:[1,0,3,2] row_mask:0xf bank_mask:0xf
	v_cndmask_b32_dpp v174, v162, v166, vcc quad_perm:[1,0,3,2] row_mask:0xf bank_mask:0xf
	v_cndmask_b32_dpp v171, v155, v159, vcc quad_perm:[1,0,3,2] row_mask:0xf bank_mask:0xf
	v_cndmask_b32_dpp v175, v163, v167, vcc quad_perm:[1,0,3,2] row_mask:0xf bank_mask:0xf
	v_cndmask_b32_dpp v172, v156, v160, vcc quad_perm:[1,0,3,2] row_mask:0xf bank_mask:0xf
	v_cndmask_b32_dpp v176, v164, v168, vcc quad_perm:[1,0,3,2] row_mask:0xf bank_mask:0xf
	v_cndmask_b32_dpp v173, v157, v161, vcc quad_perm:[1,0,3,2] row_mask:0xf bank_mask:0xf
	v_cndmask_b32_dpp v177, v165, v169, vcc quad_perm:[1,0,3,2] row_mask:0xf bank_mask:0xf
	s_mov_b32 vcc_lo, 0x55555555
	s_mov_b32 vcc_hi, 0x55555555
	s_nop 1
	v_cndmask_b32_dpp v154, v158, v154, vcc quad_perm:[1,0,3,2] row_mask:0xf bank_mask:0xf
	v_cndmask_b32_dpp v162, v166, v162, vcc quad_perm:[1,0,3,2] row_mask:0xf bank_mask:0xf
	v_cndmask_b32_dpp v155, v159, v155, vcc quad_perm:[1,0,3,2] row_mask:0xf bank_mask:0xf
	v_cndmask_b32_dpp v163, v167, v163, vcc quad_perm:[1,0,3,2] row_mask:0xf bank_mask:0xf
	v_cndmask_b32_dpp v156, v160, v156, vcc quad_perm:[1,0,3,2] row_mask:0xf bank_mask:0xf
	v_cndmask_b32_dpp v164, v168, v164, vcc quad_perm:[1,0,3,2] row_mask:0xf bank_mask:0xf
	v_cndmask_b32_dpp v157, v161, v157, vcc quad_perm:[1,0,3,2] row_mask:0xf bank_mask:0xf
	v_cndmask_b32_dpp v165, v169, v165, vcc quad_perm:[1,0,3,2] row_mask:0xf bank_mask:0xf
	s_mov_b32 vcc_lo, 0xcccccccc
	s_mov_b32 vcc_hi, 0xcccccccc
	s_nop 1
	v_cndmask_b32_dpp v158, v154, v162, vcc quad_perm:[2,3,0,1] row_mask:0xf bank_mask:0xf
	v_cndmask_b32_dpp v166, v170, v174, vcc quad_perm:[2,3,0,1] row_mask:0xf bank_mask:0xf
	v_cndmask_b32_dpp v159, v155, v163, vcc quad_perm:[2,3,0,1] row_mask:0xf bank_mask:0xf
	v_cndmask_b32_dpp v167, v171, v175, vcc quad_perm:[2,3,0,1] row_mask:0xf bank_mask:0xf
	v_cndmask_b32_dpp v160, v156, v164, vcc quad_perm:[2,3,0,1] row_mask:0xf bank_mask:0xf
	v_cndmask_b32_dpp v168, v172, v176, vcc quad_perm:[2,3,0,1] row_mask:0xf bank_mask:0xf
	v_cndmask_b32_dpp v161, v157, v165, vcc quad_perm:[2,3,0,1] row_mask:0xf bank_mask:0xf
	v_cndmask_b32_dpp v169, v173, v177, vcc quad_perm:[2,3,0,1] row_mask:0xf bank_mask:0xf
	s_mov_b32 vcc_lo, 0x33333333
	s_mov_b32 vcc_hi, 0x33333333
	s_nop 1
	v_cndmask_b32_dpp v154, v162, v154, vcc quad_perm:[2,3,0,1] row_mask:0xf bank_mask:0xf
	v_cndmask_b32_dpp v170, v174, v170, vcc quad_perm:[2,3,0,1] row_mask:0xf bank_mask:0xf
	v_cndmask_b32_dpp v155, v163, v155, vcc quad_perm:[2,3,0,1] row_mask:0xf bank_mask:0xf
	v_cndmask_b32_dpp v171, v175, v171, vcc quad_perm:[2,3,0,1] row_mask:0xf bank_mask:0xf
	v_cndmask_b32_dpp v156, v164, v156, vcc quad_perm:[2,3,0,1] row_mask:0xf bank_mask:0xf
	v_cndmask_b32_dpp v172, v176, v172, vcc quad_perm:[2,3,0,1] row_mask:0xf bank_mask:0xf
	v_cndmask_b32_dpp v157, v165, v157, vcc quad_perm:[2,3,0,1] row_mask:0xf bank_mask:0xf
	v_cndmask_b32_dpp v173, v177, v173, vcc quad_perm:[2,3,0,1] row_mask:0xf bank_mask:0xf
	global_store_dwordx4 v179, v[154:157], s[82:83] nt
	global_store_dwordx4 v180, v[170:173], s[82:83] nt
	global_store_dwordx4 v181, v[158:161], s[82:83] nt
	global_store_dwordx4 v190, v[166:169], s[82:83] nt
	v_readlane_b32 s2, v239, 0
	s_lshr_b32 s2, s2, 6
	s_add_i32 s2, s2, 13
	s_cmp_gt_u32 s2, 20
	s_cbranch_scc1 .Lhw_seam1_done
	s_add_i32 s2, s2, 21
	s_mul_i32 s2, s2, s74
	v_readlane_b32 s9, v239, 23
	s_lshr_b32 s9, s9, 3
	s_add_i32 s2, s2, s9
	s_cmp_gt_u32 s2, 24575
	s_cbranch_scc1 .Lhw_seam1_done
	v_mbcnt_lo_u32_b32 v178, -1, 0
	v_mbcnt_hi_u32_b32 v178, -1, v178
	v_and_b32_e32 v179, 60, v178
	v_lshlrev_b32_e32 v179, 10, v179
	v_and_b32_e32 v180, 3, v178
	v_lshl_or_b32 v179, v180, 4, v179
	v_add_u32_e32 v180, 0x400, v179
	v_add_u32_e32 v181, 0x800, v179
	v_add_u32_e32 v190, 0xc00, v179
	v_lshlrev_b32_e32 v178, 2, v178
	s_cmp_lt_u32 s2, 16384
	s_cbranch_scc0 .Lhw_dn_s1_2
	s_lshr_b32 s9, s2, 9
	s_bfe_u32 s32, s2, 0x40005
	s_and_b32 s53, s2, 31
	s_lshl_b32 s69, s9, 23
	s_lshl_b32 s100, s32, 19
	s_add_i32 s69, s69, s100
	s_lshl_b32 s100, s53, 8
	s_add_i32 s69, s69, s100
	s_lshl_b32 s98, s9, 11
	s_bfe_u32 s100, s53, 0x30001
	s_lshl_b32 s100, s100, 8
	s_add_i32 s98, s98, s100
	s_lshr_b32 s100, s53, 4
	s_lshl_b32 s100, s100, 7
	s_add_i32 s98, s98, s100
	s_and_b32 s100, s53, 1
	s_lshl_b32 s100, s100, 6
	s_add_i32 s98, s98, s100
	s_lshl_b32 s98, s98, 10
	s_lshl_b32 s100, s32, 6
	s_add_i32 s98, s98, s100
	s_add_i32 s98, s98, 0x2000000
	v_readlane_b32 s82, v239, 11
	v_readlane_b32 s83, v239, 12
	s_movk_i32 s89, 8192
	s_branch .Lhw_go_s1_2

.Lhw_seam2:
	s_mov_b64 exec, -1
	v_readlane_b32 s2, v239, 0
	s_lshr_b32 s2, s2, 6
	s_add_i32 s2, s2, -1
	s_cmp_gt_u32 s2, 13
	s_cbranch_scc1 .Lhw_seam2_done
	s_add_i32 s2, s2, 42
	s_mul_i32 s2, s2, s74
	v_readlane_b32 s9, v239, 23
	s_lshr_b32 s9, s9, 3
	s_add_i32 s2, s2, s9
	s_cmp_gt_u32 s2, 24575
	s_cbranch_scc1 .Lhw_seam2_done
	v_mbcnt_lo_u32_b32 v178, -1, 0
	v_mbcnt_hi_u32_b32 v178, -1, v178
	v_and_b32_e32 v179, 60, v178
	v_lshlrev_b32_e32 v179, 10, v179
	v_and_b32_e32 v180, 3, v178
	v_lshl_or_b32 v179, v180, 4, v179
	v_add_u32_e32 v180, 0x400, v179
	v_add_u32_e32 v181, 0x800, v179
	v_add_u32_e32 v190, 0xc00, v179
	v_lshlrev_b32_e32 v178, 2, v178
	s_cmp_lt_u32 s2, 16384
	s_cbranch_scc0 .Lhw_dn_s2_0
	s_lshr_b32 s9, s2, 9
	s_bfe_u32 s32, s2, 0x40005
	s_and_b32 s53, s2, 31
	s_lshl_b32 s69, s9, 23
	s_lshl_b32 s100, s32, 19
	s_add_i32 s69, s69, s100
	s_lshl_b32 s100, s53, 8
	s_add_i32 s69, s69, s100
	s_lshl_b32 s98, s9, 11
	s_bfe_u32 s100, s53, 0x30001
	s_lshl_b32 s100, s100, 8
	s_add_i32 s98, s98, s100
	s_lshr_b32 s100, s53, 4
	s_lshl_b32 s100, s100, 7
	s_add_i32 s98, s98, s100
	s_and_b32 s100, s53, 1
	s_lshl_b32 s100, s100, 6
	s_add_i32 s98, s98, s100
	s_lshl_b32 s98, s98, 10
	s_lshl_b32 s100, s32, 6
	s_add_i32 s98, s98, s100
	s_add_i32 s98, s98, 0x2000000
	v_readlane_b32 s82, v239, 11
	v_readlane_b32 s83, v239, 12
	s_movk_i32 s89, 8192
	s_branch .Lhw_go_s2_0

.Lhw_go_s2_0:
	s_add_u32 s100, s82, s69
	s_addc_u32 s101, s83, 0
	v_readlane_b32 s82, v239, 44
	v_readlane_b32 s83, v239, 45
	s_add_u32 s82, s82, s98
	s_addc_u32 s83, s83, 0
	global_load_dword v34, v178, s[100:101] nt
	s_add_u32 s100, s100, s89
	s_addc_u32 s101, s101, 0
	global_load_dword v35, v178, s[100:101] nt
	s_add_u32 s100, s100, s89
	s_addc_u32 s101, s101, 0
	global_load_dword v36, v178, s[100:101] nt
	s_add_u32 s100, s100, s89
	s_addc_u32 s101, s101, 0
	global_load_dword v37, v178, s[100:101] nt
	s_add_u32 s100, s100, s89
	s_addc_u32 s101, s101, 0
	global_load_dword v38, v178, s[100:101] nt
	s_add_u32 s100, s100, s89
	s_addc_u32 s101, s101, 0
	global_load_dword v39, v178, s[100:101] nt
	s_add_u32 s100, s100, s89
	s_addc_u32 s101, s101, 0
	global_load_dword v40, v178, s[100:101] nt
	s_add_u32 s100, s100, s89
	s_addc_u32 s101, s101, 0
	global_load_dword v41, v178, s[100:101] nt
	s_add_u32 s100, s100, s89
	s_addc_u32 s101, s101, 0
	global_load_dword v42, v178, s[100:101] nt
	s_add_u32 s100, s100, s89
	s_addc_u32 s101, s101, 0
	global_load_dword v43, v178, s[100:101] nt
	s_add_u32 s100, s100, s89
	s_addc_u32 s101, s101, 0
	global_load_dword v44, v178, s[100:101] nt
	s_add_u32 s100, s100, s89
	s_addc_u32 s101, s101, 0
	global_load_dword v45, v178, s[100:101] nt
	s_add_u32 s100, s100, s89
	s_addc_u32 s101, s101, 0
	global_load_dword v46, v178, s[100:101] nt
	s_add_u32 s100, s100, s89
	s_addc_u32 s101, s101, 0
	global_load_dword v47, v178, s[100:101] nt
	s_add_u32 s100, s100, s89
	s_addc_u32 s101, s101, 0
	global_load_dword v48, v178, s[100:101] nt
	s_add_u32 s100, s100, s89
	s_addc_u32 s101, s101, 0
	global_load_dword v49, v178, s[100:101] nt
	s_add_u32 s100, s100, s89
	s_addc_u32 s101, s101, 0
	global_load_dword v50, v178, s[100:101] nt
	s_add_u32 s100, s100, s89
	s_addc_u32 s101, s101, 0
	global_load_dword v51, v178, s[100:101] nt
	s_add_u32 s100, s100, s89
	s_addc_u32 s101, s101, 0
	global_load_dword v52, v178, s[100:101] nt
	s_add_u32 s100, s100, s89
	s_addc_u32 s101, s101, 0
	global_load_dword v53, v178, s[100:101] nt
	s_add_u32 s100, s100, s89
	s_addc_u32 s101, s101, 0
	global_load_dword v54, v178, s[100:101] nt
	s_add_u32 s100, s100, s89
	s_addc_u32 s101, s101, 0
	global_load_dword v55, v178, s[100:101] nt
	s_add_u32 s100, s100, s89
	s_addc_u32 s101, s101, 0
	global_load_dword v56, v178, s[100:101] nt
	s_add_u32 s100, s100, s89
	s_addc_u32 s101, s101, 0
	global_load_dword v57, v178, s[100:101] nt
	s_add_u32 s100, s100, s89
	s_addc_u32 s101, s101, 0
	global_load_dword v58, v178, s[100:101] nt
	s_add_u32 s100, s100, s89
	s_addc_u32 s101, s101, 0
	global_load_dword v59, v178, s[100:101] nt
	s_add_u32 s100, s100, s89
	s_addc_u32 s101, s101, 0
	global_load_dword v60, v178, s[100:101] nt
	s_add_u32 s100, s100, s89
	s_addc_u32 s101, s101, 0
	global_load_dword v61, v178, s[100:101] nt
	s_add_u32 s100, s100, s89
	s_addc_u32 s101, s101, 0
	global_load_dword v62, v178, s[100:101] nt
	s_add_u32 s100, s100, s89
	s_addc_u32 s101, s101, 0
	global_load_dword v63, v178, s[100:101] nt
	s_add_u32 s100, s100, s89
	s_addc_u32 s101, s101, 0
	global_load_dword v64, v178, s[100:101] nt
	s_add_u32 s100, s100, s89
	s_addc_u32 s101, s101, 0
	global_load_dword v65, v178, s[100:101] nt
	s_add_u32 s100, s100, s89
	s_addc_u32 s101, s101, 0
	global_load_dword v66, v178, s[100:101] nt
	s_add_u32 s100, s100, s89
	s_addc_u32 s101, s101, 0
	global_load_dword v67, v178, s[100:101] nt
	s_add_u32 s100, s100, s89
	s_addc_u32 s101, s101, 0
	global_load_dword v68, v178, s[100:101] nt
	s_add_u32 s100, s100, s89
	s_addc_u32 s101, s101, 0
	global_load_dword v69, v178, s[100:101] nt
	s_add_u32 s100, s100, s89
	s_addc_u32 s101, s101, 0
	global_load_dword v70, v178, s[100:101] nt
	s_add_u32 s100, s100, s89
	s_addc_u32 s101, s101, 0
	global_load_dword v71, v178, s[100:101] nt
	s_add_u32 s100, s100, s89
	s_addc_u32 s101, s101, 0
	global_load_dword v72, v178, s[100:101] nt
	s_add_u32 s100, s100, s89
	s_addc_u32 s101, s101, 0
	global_load_dword v73, v178, s[100:101] nt
	s_add_u32 s100, s100, s89
	s_addc_u32 s101, s101, 0
	global_load_dword v74, v178, s[100:101] nt
	s_add_u32 s100, s100, s89
	s_addc_u32 s101, s101, 0
	global_load_dword v75, v178, s[100:101] nt
	s_add_u32 s100, s100, s89
	s_addc_u32 s101, s101, 0
	global_load_dword v76, v178, s[100:101] nt
	s_add_u32 s100, s100, s89
	s_addc_u32 s101, s101, 0
	global_load_dword v77, v178, s[100:101] nt
	s_add_u32 s100, s100, s89
	s_addc_u32 s101, s101, 0
	global_load_dword v78, v178, s[100:101] nt
	s_add_u32 s100, s100, s89
	s_addc_u32 s101, s101, 0
	global_load_dword v79, v178, s[100:101] nt
	s_add_u32 s100, s100, s89
	s_addc_u32 s101, s101, 0
	global_load_dword v80, v178, s[100:101] nt
	s_add_u32 s100, s100, s89
	s_addc_u32 s101, s101, 0
	global_load_dword v81, v178, s[100:101] nt
	s_add_u32 s100, s100, s89
	s_addc_u32 s101, s101, 0
	global_load_dword v82, v178, s[100:101] nt
	s_add_u32 s100, s100, s89
	s_addc_u32 s101, s101, 0
	global_load_dword v83, v178, s[100:101] nt
	s_add_u32 s100, s100, s89
	s_addc_u32 s101, s101, 0
	global_load_dword v84, v178, s[100:101] nt
	s_add_u32 s100, s100, s89
	s_addc_u32 s101, s101, 0
	global_load_dword v85, v178, s[100:101] nt
	s_add_u32 s100, s100, s89
	s_addc_u32 s101, s101, 0
	global_load_dword v86, v178, s[100:101] nt
	s_add_u32 s100, s100, s89
	s_addc_u32 s101, s101, 0
	global_load_dword v87, v178, s[100:101] nt
	s_add_u32 s100, s100, s89
	s_addc_u32 s101, s101, 0
	global_load_dword v88, v178, s[100:101] nt
	s_add_u32 s100, s100, s89
	s_addc_u32 s101, s101, 0
	global_load_dword v89, v178, s[100:101] nt
	s_add_u32 s100, s100, s89
	s_addc_u32 s101, s101, 0
	global_load_dword v90, v178, s[100:101] nt
	s_add_u32 s100, s100, s89
	s_addc_u32 s101, s101, 0
	global_load_dword v91, v178, s[100:101] nt
	s_add_u32 s100, s100, s89
	s_addc_u32 s101, s101, 0
	global_load_dword v92, v178, s[100:101] nt
	s_add_u32 s100, s100, s89
	s_addc_u32 s101, s101, 0
	global_load_dword v93, v178, s[100:101] nt
	s_add_u32 s100, s100, s89
	s_addc_u32 s101, s101, 0
	global_load_dword v94, v178, s[100:101] nt
	s_add_u32 s100, s100, s89
	s_addc_u32 s101, s101, 0
	global_load_dword v95, v178, s[100:101] nt
	s_add_u32 s100, s100, s89
	s_addc_u32 s101, s101, 0
	global_load_dword v96, v178, s[100:101] nt
	s_add_u32 s100, s100, s89
	s_addc_u32 s101, s101, 0
	global_load_dword v97, v178, s[100:101] nt
	s_add_u32 s100, s100, s89
	s_addc_u32 s101, s101, 0
	s_waitcnt vmcnt(48)
	v_mul_f32_e32 v34, 0x42000000, v34
	v_mul_f32_e32 v35, 0x42000000, v35
	v_mul_f32_e32 v36, 0x42000000, v36
	v_mul_f32_e32 v37, 0x42000000, v37
	v_mul_f32_e32 v38, 0x42000000, v38
	v_mul_f32_e32 v39, 0x42000000, v39
	v_mul_f32_e32 v40, 0x42000000, v40
	v_mul_f32_e32 v41, 0x42000000, v41
	v_mul_f32_e32 v42, 0x42000000, v42
	v_mul_f32_e32 v43, 0x42000000, v43
	v_mul_f32_e32 v44, 0x42000000, v44
	v_mul_f32_e32 v45, 0x42000000, v45
	v_mul_f32_e32 v46, 0x42000000, v46
	v_mul_f32_e32 v47, 0x42000000, v47
	v_mul_f32_e32 v48, 0x42000000, v48
	v_mul_f32_e32 v49, 0x42000000, v49
	v_cvt_pk_fp8_f32 v154, v34, v35
	v_cvt_pk_fp8_f32 v155, v38, v39
	v_cvt_pk_fp8_f32 v156, v42, v43
	v_cvt_pk_fp8_f32 v157, v46, v47
	v_cvt_pk_fp8_f32 v154, v36, v37 op_sel:[0,0,1]
	v_cvt_pk_fp8_f32 v155, v40, v41 op_sel:[0,0,1]
	v_cvt_pk_fp8_f32 v156, v44, v45 op_sel:[0,0,1]
	v_cvt_pk_fp8_f32 v157, v48, v49 op_sel:[0,0,1]
	s_waitcnt vmcnt(32)
	v_mul_f32_e32 v50, 0x42000000, v50
	v_mul_f32_e32 v51, 0x42000000, v51
	v_mul_f32_e32 v52, 0x42000000, v52
	v_mul_f32_e32 v53, 0x42000000, v53
	v_mul_f32_e32 v54, 0x42000000, v54
	v_mul_f32_e32 v55, 0x42000000, v55
	v_mul_f32_e32 v56, 0x42000000, v56
	v_mul_f32_e32 v57, 0x42000000, v57
	v_mul_f32_e32 v58, 0x42000000, v58
	v_mul_f32_e32 v59, 0x42000000, v59
	v_mul_f32_e32 v60, 0x42000000, v60
	v_mul_f32_e32 v61, 0x42000000, v61
	v_mul_f32_e32 v62, 0x42000000, v62
	v_mul_f32_e32 v63, 0x42000000, v63
	v_mul_f32_e32 v64, 0x42000000, v64
	v_mul_f32_e32 v65, 0x42000000, v65
	v_cvt_pk_fp8_f32 v158, v50, v51
	v_cvt_pk_fp8_f32 v159, v54, v55
	v_cvt_pk_fp8_f32 v160, v58, v59
	v_cvt_pk_fp8_f32 v161, v62, v63
	v_cvt_pk_fp8_f32 v158, v52, v53 op_sel:[0,0,1]
	v_cvt_pk_fp8_f32 v159, v56, v57 op_sel:[0,0,1]
	v_cvt_pk_fp8_f32 v160, v60, v61 op_sel:[0,0,1]
	v_cvt_pk_fp8_f32 v161, v64, v65 op_sel:[0,0,1]
	s_waitcnt vmcnt(16)
	v_mul_f32_e32 v66, 0x42000000, v66
	v_mul_f32_e32 v67, 0x42000000, v67
	v_mul_f32_e32 v68, 0x42000000, v68
	v_mul_f32_e32 v69, 0x42000000, v69
	v_mul_f32_e32 v70, 0x42000000, v70
	v_mul_f32_e32 v71, 0x42000000, v71
	v_mul_f32_e32 v72, 0x42000000, v72
	v_mul_f32_e32 v73, 0x42000000, v73
	v_mul_f32_e32 v74, 0x42000000, v74
	v_mul_f32_e32 v75, 0x42000000, v75
	v_mul_f32_e32 v76, 0x42000000, v76
	v_mul_f32_e32 v77, 0x42000000, v77
	v_mul_f32_e32 v78, 0x42000000, v78
	v_mul_f32_e32 v79, 0x42000000, v79
	v_mul_f32_e32 v80, 0x42000000, v80
	v_mul_f32_e32 v81, 0x42000000, v81
	v_cvt_pk_fp8_f32 v162, v66, v67
	v_cvt_pk_fp8_f32 v163, v70, v71
	v_cvt_pk_fp8_f32 v164, v74, v75
	v_cvt_pk_fp8_f32 v165, v78, v79
	v_cvt_pk_fp8_f32 v162, v68, v69 op_sel:[0,0,1]
	v_cvt_pk_fp8_f32 v163, v72, v73 op_sel:[0,0,1]
	v_cvt_pk_fp8_f32 v164, v76, v77 op_sel:[0,0,1]
	v_cvt_pk_fp8_f32 v165, v80, v81 op_sel:[0,0,1]
	s_waitcnt vmcnt(0)
	v_mul_f32_e32 v82, 0x42000000, v82
	v_mul_f32_e32 v83, 0x42000000, v83
	v_mul_f32_e32 v84, 0x42000000, v84
	v_mul_f32_e32 v85, 0x42000000, v85
	v_mul_f32_e32 v86, 0x42000000, v86
	v_mul_f32_e32 v87, 0x42000000, v87
	v_mul_f32_e32 v88, 0x42000000, v88
	v_mul_f32_e32 v89, 0x42000000, v89
	v_mul_f32_e32 v90, 0x42000000, v90
	v_mul_f32_e32 v91, 0x42000000, v91
	v_mul_f32_e32 v92, 0x42000000, v92
	v_mul_f32_e32 v93, 0x42000000, v93
	v_mul_f32_e32 v94, 0x42000000, v94
	v_mul_f32_e32 v95, 0x42000000, v95
	v_mul_f32_e32 v96, 0x42000000, v96
	v_mul_f32_e32 v97, 0x42000000, v97
	v_cvt_pk_fp8_f32 v166, v82, v83
	v_cvt_pk_fp8_f32 v167, v86, v87
	v_cvt_pk_fp8_f32 v168, v90, v91
	v_cvt_pk_fp8_f32 v169, v94, v95
	v_cvt_pk_fp8_f32 v166, v84, v85 op_sel:[0,0,1]
	v_cvt_pk_fp8_f32 v167, v88, v89 op_sel:[0,0,1]
	v_cvt_pk_fp8_f32 v168, v92, v93 op_sel:[0,0,1]
	v_cvt_pk_fp8_f32 v169, v96, v97 op_sel:[0,0,1]
	s_mov_b32 vcc_lo, 0xaaaaaaaa
	s_mov_b32 vcc_hi, 0xaaaaaaaa
	s_nop 1
	v_cndmask_b32_dpp v170, v154, v158, vcc quad_perm:[1,0,3,2] row_mask:0xf bank_mask:0xf
	v_cndmask_b32_dpp v174, v162, v166, vcc quad_perm:[1,0,3,2] row_mask:0xf bank_mask:0xf
	v_cndmask_b32_dpp v171, v155, v159, vcc quad_perm:[1,0,3,2] row_mask:0xf bank_mask:0xf
	v_cndmask_b32_dpp v175, v163, v167, vcc quad_perm:[1,0,3,2] row_mask:0xf bank_mask:0xf
	v_cndmask_b32_dpp v172, v156, v160, vcc quad_perm:[1,0,3,2] row_mask:0xf bank_mask:0xf
	v_cndmask_b32_dpp v176, v164, v168, vcc quad_perm:[1,0,3,2] row_mask:0xf bank_mask:0xf
	v_cndmask_b32_dpp v173, v157, v161, vcc quad_perm:[1,0,3,2] row_mask:0xf bank_mask:0xf
	v_cndmask_b32_dpp v177, v165, v169, vcc quad_perm:[1,0,3,2] row_mask:0xf bank_mask:0xf
	s_mov_b32 vcc_lo, 0x55555555
	s_mov_b32 vcc_hi, 0x55555555
	s_nop 1
	v_cndmask_b32_dpp v154, v158, v154, vcc quad_perm:[1,0,3,2] row_mask:0xf bank_mask:0xf
	v_cndmask_b32_dpp v162, v166, v162, vcc quad_perm:[1,0,3,2] row_mask:0xf bank_mask:0xf
	v_cndmask_b32_dpp v155, v159, v155, vcc quad_perm:[1,0,3,2] row_mask:0xf bank_mask:0xf
	v_cndmask_b32_dpp v163, v167, v163, vcc quad_perm:[1,0,3,2] row_mask:0xf bank_mask:0xf
	v_cndmask_b32_dpp v156, v160, v156, vcc quad_perm:[1,0,3,2] row_mask:0xf bank_mask:0xf
	v_cndmask_b32_dpp v164, v168, v164, vcc quad_perm:[1,0,3,2] row_mask:0xf bank_mask:0xf
	v_cndmask_b32_dpp v157, v161, v157, vcc quad_perm:[1,0,3,2] row_mask:0xf bank_mask:0xf
	v_cndmask_b32_dpp v165, v169, v165, vcc quad_perm:[1,0,3,2] row_mask:0xf bank_mask:0xf
	s_mov_b32 vcc_lo, 0xcccccccc
	s_mov_b32 vcc_hi, 0xcccccccc
	s_nop 1
	v_cndmask_b32_dpp v158, v154, v162, vcc quad_perm:[2,3,0,1] row_mask:0xf bank_mask:0xf
	v_cndmask_b32_dpp v166, v170, v174, vcc quad_perm:[2,3,0,1] row_mask:0xf bank_mask:0xf
	v_cndmask_b32_dpp v159, v155, v163, vcc quad_perm:[2,3,0,1] row_mask:0xf bank_mask:0xf
	v_cndmask_b32_dpp v167, v171, v175, vcc quad_perm:[2,3,0,1] row_mask:0xf bank_mask:0xf
	v_cndmask_b32_dpp v160, v156, v164, vcc quad_perm:[2,3,0,1] row_mask:0xf bank_mask:0xf
	v_cndmask_b32_dpp v168, v172, v176, vcc quad_perm:[2,3,0,1] row_mask:0xf bank_mask:0xf
	v_cndmask_b32_dpp v161, v157, v165, vcc quad_perm:[2,3,0,1] row_mask:0xf bank_mask:0xf
	v_cndmask_b32_dpp v169, v173, v177, vcc quad_perm:[2,3,0,1] row_mask:0xf bank_mask:0xf
	s_mov_b32 vcc_lo, 0x33333333
	s_mov_b32 vcc_hi, 0x33333333
	s_nop 1
	v_cndmask_b32_dpp v154, v162, v154, vcc quad_perm:[2,3,0,1] row_mask:0xf bank_mask:0xf
	v_cndmask_b32_dpp v170, v174, v170, vcc quad_perm:[2,3,0,1] row_mask:0xf bank_mask:0xf
	v_cndmask_b32_dpp v155, v163, v155, vcc quad_perm:[2,3,0,1] row_mask:0xf bank_mask:0xf
	v_cndmask_b32_dpp v171, v175, v171, vcc quad_perm:[2,3,0,1] row_mask:0xf bank_mask:0xf
	v_cndmask_b32_dpp v156, v164, v156, vcc quad_perm:[2,3,0,1] row_mask:0xf bank_mask:0xf
	v_cndmask_b32_dpp v172, v176, v172, vcc quad_perm:[2,3,0,1] row_mask:0xf bank_mask:0xf
	v_cndmask_b32_dpp v157, v165, v157, vcc quad_perm:[2,3,0,1] row_mask:0xf bank_mask:0xf
	v_cndmask_b32_dpp v173, v177, v173, vcc quad_perm:[2,3,0,1] row_mask:0xf bank_mask:0xf
	global_store_dwordx4 v179, v[154:157], s[82:83] nt
	global_store_dwordx4 v180, v[170:173], s[82:83] nt
	global_store_dwordx4 v181, v[158:161], s[82:83] nt
	global_store_dwordx4 v190, v[166:169], s[82:83] nt
	v_readlane_b32 s2, v239, 0
	s_lshr_b32 s2, s2, 6
	s_add_i32 s2, s2, 6
	s_cmp_gt_u32 s2, 13
	s_cbranch_scc1 .Lhw_seam2_done
	s_add_i32 s2, s2, 42
	s_mul_i32 s2, s2, s74
	v_readlane_b32 s9, v239, 23
	s_lshr_b32 s9, s9, 3
	s_add_i32 s2, s2, s9
	s_cmp_gt_u32 s2, 24575
	s_cbranch_scc1 .Lhw_seam2_done
	v_mbcnt_lo_u32_b32 v178, -1, 0
	v_mbcnt_hi_u32_b32 v178, -1, v178
	v_and_b32_e32 v179, 60, v178
	v_lshlrev_b32_e32 v179, 10, v179
	v_and_b32_e32 v180, 3, v178
	v_lshl_or_b32 v179, v180, 4, v179
	v_add_u32_e32 v180, 0x400, v179
	v_add_u32_e32 v181, 0x800, v179
	v_add_u32_e32 v190, 0xc00, v179
	v_lshlrev_b32_e32 v178, 2, v178
	s_cmp_lt_u32 s2, 16384
	s_cbranch_scc0 .Lhw_dn_s2_1
	s_lshr_b32 s9, s2, 9
	s_bfe_u32 s32, s2, 0x40005
	s_and_b32 s53, s2, 31
	s_lshl_b32 s69, s9, 23
	s_lshl_b32 s100, s32, 19
	s_add_i32 s69, s69, s100
	s_lshl_b32 s100, s53, 8
	s_add_i32 s69, s69, s100
	s_lshl_b32 s98, s9, 11
	s_bfe_u32 s100, s53, 0x30001
	s_lshl_b32 s100, s100, 8
	s_add_i32 s98, s98, s100
	s_lshr_b32 s100, s53, 4
	s_lshl_b32 s100, s100, 7
	s_add_i32 s98, s98, s100
	s_and_b32 s100, s53, 1
	s_lshl_b32 s100, s100, 6
	s_add_i32 s98, s98, s100
	s_lshl_b32 s98, s98, 10
	s_lshl_b32 s100, s32, 6
	s_add_i32 s98, s98, s100
	s_add_i32 s98, s98, 0x2000000
	v_readlane_b32 s82, v239, 11
	v_readlane_b32 s83, v239, 12
	s_movk_i32 s89, 8192
	s_branch .Lhw_go_s2_1

.Lhw_seam3:
	s_mov_b64 exec, -1
	v_readlane_b32 s2, v239, 0
	s_lshr_b32 s2, s2, 6
	s_add_i32 s2, s2, -1
	s_cmp_gt_u32 s2, 13
	s_cbranch_scc1 .Lhw_seam3_done
	s_add_i32 s2, s2, 56
	s_mul_i32 s2, s2, s74
	v_readlane_b32 s9, v239, 23
	s_lshr_b32 s9, s9, 3
	s_add_i32 s2, s2, s9
	s_cmp_gt_u32 s2, 24575
	s_cbranch_scc1 .Lhw_seam3_done
	v_mbcnt_lo_u32_b32 v178, -1, 0
	v_mbcnt_hi_u32_b32 v178, -1, v178
	v_and_b32_e32 v179, 60, v178
	v_lshlrev_b32_e32 v179, 10, v179
	v_and_b32_e32 v180, 3, v178
	v_lshl_or_b32 v179, v180, 4, v179
	v_add_u32_e32 v180, 0x400, v179
	v_add_u32_e32 v181, 0x800, v179
	v_add_u32_e32 v190, 0xc00, v179
	v_lshlrev_b32_e32 v178, 2, v178
	s_cmp_lt_u32 s2, 16384
	s_cbranch_scc0 .Lhw_dn_s3_0
	s_lshr_b32 s9, s2, 9
	s_bfe_u32 s32, s2, 0x40005
	s_and_b32 s53, s2, 31
	s_lshl_b32 s69, s9, 23
	s_lshl_b32 s100, s32, 19
	s_add_i32 s69, s69, s100
	s_lshl_b32 s100, s53, 8
	s_add_i32 s69, s69, s100
	s_lshl_b32 s98, s9, 11
	s_bfe_u32 s100, s53, 0x30001
	s_lshl_b32 s100, s100, 8
	s_add_i32 s98, s98, s100
	s_lshr_b32 s100, s53, 4
	s_lshl_b32 s100, s100, 7
	s_add_i32 s98, s98, s100
	s_and_b32 s100, s53, 1
	s_lshl_b32 s100, s100, 6
	s_add_i32 s98, s98, s100
	s_lshl_b32 s98, s98, 10
	s_lshl_b32 s100, s32, 6
	s_add_i32 s98, s98, s100
	s_add_i32 s98, s98, 0x2000000
	v_readlane_b32 s82, v239, 11
	v_readlane_b32 s83, v239, 12
	s_movk_i32 s89, 8192
	s_branch .Lhw_go_s3_0

.Lhw_go_s3_0:
	s_add_u32 s100, s82, s69
	s_addc_u32 s101, s83, 0
	v_readlane_b32 s82, v239, 44
	v_readlane_b32 s83, v239, 45
	s_add_u32 s82, s82, s98
	s_addc_u32 s83, s83, 0
	global_load_dword v34, v178, s[100:101] nt
	s_add_u32 s100, s100, s89
	s_addc_u32 s101, s101, 0
	global_load_dword v35, v178, s[100:101] nt
	s_add_u32 s100, s100, s89
	s_addc_u32 s101, s101, 0
	global_load_dword v36, v178, s[100:101] nt
	s_add_u32 s100, s100, s89
	s_addc_u32 s101, s101, 0
	global_load_dword v37, v178, s[100:101] nt
	s_add_u32 s100, s100, s89
	s_addc_u32 s101, s101, 0
	global_load_dword v38, v178, s[100:101] nt
	s_add_u32 s100, s100, s89
	s_addc_u32 s101, s101, 0
	global_load_dword v39, v178, s[100:101] nt
	s_add_u32 s100, s100, s89
	s_addc_u32 s101, s101, 0
	global_load_dword v40, v178, s[100:101] nt
	s_add_u32 s100, s100, s89
	s_addc_u32 s101, s101, 0
	global_load_dword v41, v178, s[100:101] nt
	s_add_u32 s100, s100, s89
	s_addc_u32 s101, s101, 0
	global_load_dword v42, v178, s[100:101] nt
	s_add_u32 s100, s100, s89
	s_addc_u32 s101, s101, 0
	global_load_dword v43, v178, s[100:101] nt
	s_add_u32 s100, s100, s89
	s_addc_u32 s101, s101, 0
	global_load_dword v44, v178, s[100:101] nt
	s_add_u32 s100, s100, s89
	s_addc_u32 s101, s101, 0
	global_load_dword v45, v178, s[100:101] nt
	s_add_u32 s100, s100, s89
	s_addc_u32 s101, s101, 0
	global_load_dword v46, v178, s[100:101] nt
	s_add_u32 s100, s100, s89
	s_addc_u32 s101, s101, 0
	global_load_dword v47, v178, s[100:101] nt
	s_add_u32 s100, s100, s89
	s_addc_u32 s101, s101, 0
	global_load_dword v48, v178, s[100:101] nt
	s_add_u32 s100, s100, s89
	s_addc_u32 s101, s101, 0
	global_load_dword v49, v178, s[100:101] nt
	s_add_u32 s100, s100, s89
	s_addc_u32 s101, s101, 0
	global_load_dword v50, v178, s[100:101] nt
	s_add_u32 s100, s100, s89
	s_addc_u32 s101, s101, 0
	global_load_dword v51, v178, s[100:101] nt
	s_add_u32 s100, s100, s89
	s_addc_u32 s101, s101, 0
	global_load_dword v52, v178, s[100:101] nt
	s_add_u32 s100, s100, s89
	s_addc_u32 s101, s101, 0
	global_load_dword v53, v178, s[100:101] nt
	s_add_u32 s100, s100, s89
	s_addc_u32 s101, s101, 0
	global_load_dword v54, v178, s[100:101] nt
	s_add_u32 s100, s100, s89
	s_addc_u32 s101, s101, 0
	global_load_dword v55, v178, s[100:101] nt
	s_add_u32 s100, s100, s89
	s_addc_u32 s101, s101, 0
	global_load_dword v56, v178, s[100:101] nt
	s_add_u32 s100, s100, s89
	s_addc_u32 s101, s101, 0
	global_load_dword v57, v178, s[100:101] nt
	s_add_u32 s100, s100, s89
	s_addc_u32 s101, s101, 0
	global_load_dword v58, v178, s[100:101] nt
	s_add_u32 s100, s100, s89
	s_addc_u32 s101, s101, 0
	global_load_dword v59, v178, s[100:101] nt
	s_add_u32 s100, s100, s89
	s_addc_u32 s101, s101, 0
	global_load_dword v60, v178, s[100:101] nt
	s_add_u32 s100, s100, s89
	s_addc_u32 s101, s101, 0
	global_load_dword v61, v178, s[100:101] nt
	s_add_u32 s100, s100, s89
	s_addc_u32 s101, s101, 0
	global_load_dword v62, v178, s[100:101] nt
	s_add_u32 s100, s100, s89
	s_addc_u32 s101, s101, 0
	global_load_dword v63, v178, s[100:101] nt
	s_add_u32 s100, s100, s89
	s_addc_u32 s101, s101, 0
	global_load_dword v64, v178, s[100:101] nt
	s_add_u32 s100, s100, s89
	s_addc_u32 s101, s101, 0
	global_load_dword v65, v178, s[100:101] nt
	s_add_u32 s100, s100, s89
	s_addc_u32 s101, s101, 0
	global_load_dword v66, v178, s[100:101] nt
	s_add_u32 s100, s100, s89
	s_addc_u32 s101, s101, 0
	global_load_dword v67, v178, s[100:101] nt
	s_add_u32 s100, s100, s89
	s_addc_u32 s101, s101, 0
	global_load_dword v68, v178, s[100:101] nt
	s_add_u32 s100, s100, s89
	s_addc_u32 s101, s101, 0
	global_load_dword v69, v178, s[100:101] nt
	s_add_u32 s100, s100, s89
	s_addc_u32 s101, s101, 0
	global_load_dword v70, v178, s[100:101] nt
	s_add_u32 s100, s100, s89
	s_addc_u32 s101, s101, 0
	global_load_dword v71, v178, s[100:101] nt
	s_add_u32 s100, s100, s89
	s_addc_u32 s101, s101, 0
	global_load_dword v72, v178, s[100:101] nt
	s_add_u32 s100, s100, s89
	s_addc_u32 s101, s101, 0
	global_load_dword v73, v178, s[100:101] nt
	s_add_u32 s100, s100, s89
	s_addc_u32 s101, s101, 0
	global_load_dword v74, v178, s[100:101] nt
	s_add_u32 s100, s100, s89
	s_addc_u32 s101, s101, 0
	global_load_dword v75, v178, s[100:101] nt
	s_add_u32 s100, s100, s89
	s_addc_u32 s101, s101, 0
	global_load_dword v76, v178, s[100:101] nt
	s_add_u32 s100, s100, s89
	s_addc_u32 s101, s101, 0
	global_load_dword v77, v178, s[100:101] nt
	s_add_u32 s100, s100, s89
	s_addc_u32 s101, s101, 0
	global_load_dword v78, v178, s[100:101] nt
	s_add_u32 s100, s100, s89
	s_addc_u32 s101, s101, 0
	global_load_dword v79, v178, s[100:101] nt
	s_add_u32 s100, s100, s89
	s_addc_u32 s101, s101, 0
	global_load_dword v80, v178, s[100:101] nt
	s_add_u32 s100, s100, s89
	s_addc_u32 s101, s101, 0
	global_load_dword v81, v178, s[100:101] nt
	s_add_u32 s100, s100, s89
	s_addc_u32 s101, s101, 0
	global_load_dword v82, v178, s[100:101] nt
	s_add_u32 s100, s100, s89
	s_addc_u32 s101, s101, 0
	global_load_dword v83, v178, s[100:101] nt
	s_add_u32 s100, s100, s89
	s_addc_u32 s101, s101, 0
	global_load_dword v84, v178, s[100:101] nt
	s_add_u32 s100, s100, s89
	s_addc_u32 s101, s101, 0
	global_load_dword v85, v178, s[100:101] nt
	s_add_u32 s100, s100, s89
	s_addc_u32 s101, s101, 0
	global_load_dword v86, v178, s[100:101] nt
	s_add_u32 s100, s100, s89
	s_addc_u32 s101, s101, 0
	global_load_dword v87, v178, s[100:101] nt
	s_add_u32 s100, s100, s89
	s_addc_u32 s101, s101, 0
	global_load_dword v88, v178, s[100:101] nt
	s_add_u32 s100, s100, s89
	s_addc_u32 s101, s101, 0
	global_load_dword v89, v178, s[100:101] nt
	s_add_u32 s100, s100, s89
	s_addc_u32 s101, s101, 0
	global_load_dword v90, v178, s[100:101] nt
	s_add_u32 s100, s100, s89
	s_addc_u32 s101, s101, 0
	global_load_dword v91, v178, s[100:101] nt
	s_add_u32 s100, s100, s89
	s_addc_u32 s101, s101, 0
	global_load_dword v92, v178, s[100:101] nt
	s_add_u32 s100, s100, s89
	s_addc_u32 s101, s101, 0
	global_load_dword v93, v178, s[100:101] nt
	s_add_u32 s100, s100, s89
	s_addc_u32 s101, s101, 0
	global_load_dword v94, v178, s[100:101] nt
	s_add_u32 s100, s100, s89
	s_addc_u32 s101, s101, 0
	global_load_dword v95, v178, s[100:101] nt
	s_add_u32 s100, s100, s89
	s_addc_u32 s101, s101, 0
	global_load_dword v96, v178, s[100:101] nt
	s_add_u32 s100, s100, s89
	s_addc_u32 s101, s101, 0
	global_load_dword v97, v178, s[100:101] nt
	s_add_u32 s100, s100, s89
	s_addc_u32 s101, s101, 0
	s_waitcnt vmcnt(48)
	v_mul_f32_e32 v34, 0x42000000, v34
	v_mul_f32_e32 v35, 0x42000000, v35
	v_mul_f32_e32 v36, 0x42000000, v36
	v_mul_f32_e32 v37, 0x42000000, v37
	v_mul_f32_e32 v38, 0x42000000, v38
	v_mul_f32_e32 v39, 0x42000000, v39
	v_mul_f32_e32 v40, 0x42000000, v40
	v_mul_f32_e32 v41, 0x42000000, v41
	v_mul_f32_e32 v42, 0x42000000, v42
	v_mul_f32_e32 v43, 0x42000000, v43
	v_mul_f32_e32 v44, 0x42000000, v44
	v_mul_f32_e32 v45, 0x42000000, v45
	v_mul_f32_e32 v46, 0x42000000, v46
	v_mul_f32_e32 v47, 0x42000000, v47
	v_mul_f32_e32 v48, 0x42000000, v48
	v_mul_f32_e32 v49, 0x42000000, v49
	v_cvt_pk_fp8_f32 v154, v34, v35
	v_cvt_pk_fp8_f32 v155, v38, v39
	v_cvt_pk_fp8_f32 v156, v42, v43
	v_cvt_pk_fp8_f32 v157, v46, v47
	v_cvt_pk_fp8_f32 v154, v36, v37 op_sel:[0,0,1]
	v_cvt_pk_fp8_f32 v155, v40, v41 op_sel:[0,0,1]
	v_cvt_pk_fp8_f32 v156, v44, v45 op_sel:[0,0,1]
	v_cvt_pk_fp8_f32 v157, v48, v49 op_sel:[0,0,1]
	s_waitcnt vmcnt(32)
	v_mul_f32_e32 v50, 0x42000000, v50
	v_mul_f32_e32 v51, 0x42000000, v51
	v_mul_f32_e32 v52, 0x42000000, v52
	v_mul_f32_e32 v53, 0x42000000, v53
	v_mul_f32_e32 v54, 0x42000000, v54
	v_mul_f32_e32 v55, 0x42000000, v55
	v_mul_f32_e32 v56, 0x42000000, v56
	v_mul_f32_e32 v57, 0x42000000, v57
	v_mul_f32_e32 v58, 0x42000000, v58
	v_mul_f32_e32 v59, 0x42000000, v59
	v_mul_f32_e32 v60, 0x42000000, v60
	v_mul_f32_e32 v61, 0x42000000, v61
	v_mul_f32_e32 v62, 0x42000000, v62
	v_mul_f32_e32 v63, 0x42000000, v63
	v_mul_f32_e32 v64, 0x42000000, v64
	v_mul_f32_e32 v65, 0x42000000, v65
	v_cvt_pk_fp8_f32 v158, v50, v51
	v_cvt_pk_fp8_f32 v159, v54, v55
	v_cvt_pk_fp8_f32 v160, v58, v59
	v_cvt_pk_fp8_f32 v161, v62, v63
	v_cvt_pk_fp8_f32 v158, v52, v53 op_sel:[0,0,1]
	v_cvt_pk_fp8_f32 v159, v56, v57 op_sel:[0,0,1]
	v_cvt_pk_fp8_f32 v160, v60, v61 op_sel:[0,0,1]
	v_cvt_pk_fp8_f32 v161, v64, v65 op_sel:[0,0,1]
	s_waitcnt vmcnt(16)
	v_mul_f32_e32 v66, 0x42000000, v66
	v_mul_f32_e32 v67, 0x42000000, v67
	v_mul_f32_e32 v68, 0x42000000, v68
	v_mul_f32_e32 v69, 0x42000000, v69
	v_mul_f32_e32 v70, 0x42000000, v70
	v_mul_f32_e32 v71, 0x42000000, v71
	v_mul_f32_e32 v72, 0x42000000, v72
	v_mul_f32_e32 v73, 0x42000000, v73
	v_mul_f32_e32 v74, 0x42000000, v74
	v_mul_f32_e32 v75, 0x42000000, v75
	v_mul_f32_e32 v76, 0x42000000, v76
	v_mul_f32_e32 v77, 0x42000000, v77
	v_mul_f32_e32 v78, 0x42000000, v78
	v_mul_f32_e32 v79, 0x42000000, v79
	v_mul_f32_e32 v80, 0x42000000, v80
	v_mul_f32_e32 v81, 0x42000000, v81
	v_cvt_pk_fp8_f32 v162, v66, v67
	v_cvt_pk_fp8_f32 v163, v70, v71
	v_cvt_pk_fp8_f32 v164, v74, v75
	v_cvt_pk_fp8_f32 v165, v78, v79
	v_cvt_pk_fp8_f32 v162, v68, v69 op_sel:[0,0,1]
	v_cvt_pk_fp8_f32 v163, v72, v73 op_sel:[0,0,1]
	v_cvt_pk_fp8_f32 v164, v76, v77 op_sel:[0,0,1]
	v_cvt_pk_fp8_f32 v165, v80, v81 op_sel:[0,0,1]
	s_waitcnt vmcnt(0)
	v_mul_f32_e32 v82, 0x42000000, v82
	v_mul_f32_e32 v83, 0x42000000, v83
	v_mul_f32_e32 v84, 0x42000000, v84
	v_mul_f32_e32 v85, 0x42000000, v85
	v_mul_f32_e32 v86, 0x42000000, v86
	v_mul_f32_e32 v87, 0x42000000, v87
	v_mul_f32_e32 v88, 0x42000000, v88
	v_mul_f32_e32 v89, 0x42000000, v89
	v_mul_f32_e32 v90, 0x42000000, v90
	v_mul_f32_e32 v91, 0x42000000, v91
	v_mul_f32_e32 v92, 0x42000000, v92
	v_mul_f32_e32 v93, 0x42000000, v93
	v_mul_f32_e32 v94, 0x42000000, v94
	v_mul_f32_e32 v95, 0x42000000, v95
	v_mul_f32_e32 v96, 0x42000000, v96
	v_mul_f32_e32 v97, 0x42000000, v97
	v_cvt_pk_fp8_f32 v166, v82, v83
	v_cvt_pk_fp8_f32 v167, v86, v87
	v_cvt_pk_fp8_f32 v168, v90, v91
	v_cvt_pk_fp8_f32 v169, v94, v95
	v_cvt_pk_fp8_f32 v166, v84, v85 op_sel:[0,0,1]
	v_cvt_pk_fp8_f32 v167, v88, v89 op_sel:[0,0,1]
	v_cvt_pk_fp8_f32 v168, v92, v93 op_sel:[0,0,1]
	v_cvt_pk_fp8_f32 v169, v96, v97 op_sel:[0,0,1]
	s_mov_b32 vcc_lo, 0xaaaaaaaa
	s_mov_b32 vcc_hi, 0xaaaaaaaa
	s_nop 1
	v_cndmask_b32_dpp v170, v154, v158, vcc quad_perm:[1,0,3,2] row_mask:0xf bank_mask:0xf
	v_cndmask_b32_dpp v174, v162, v166, vcc quad_perm:[1,0,3,2] row_mask:0xf bank_mask:0xf
	v_cndmask_b32_dpp v171, v155, v159, vcc quad_perm:[1,0,3,2] row_mask:0xf bank_mask:0xf
	v_cndmask_b32_dpp v175, v163, v167, vcc quad_perm:[1,0,3,2] row_mask:0xf bank_mask:0xf
	v_cndmask_b32_dpp v172, v156, v160, vcc quad_perm:[1,0,3,2] row_mask:0xf bank_mask:0xf
	v_cndmask_b32_dpp v176, v164, v168, vcc quad_perm:[1,0,3,2] row_mask:0xf bank_mask:0xf
	v_cndmask_b32_dpp v173, v157, v161, vcc quad_perm:[1,0,3,2] row_mask:0xf bank_mask:0xf
	v_cndmask_b32_dpp v177, v165, v169, vcc quad_perm:[1,0,3,2] row_mask:0xf bank_mask:0xf
	s_mov_b32 vcc_lo, 0x55555555
	s_mov_b32 vcc_hi, 0x55555555
	s_nop 1
	v_cndmask_b32_dpp v154, v158, v154, vcc quad_perm:[1,0,3,2] row_mask:0xf bank_mask:0xf
	v_cndmask_b32_dpp v162, v166, v162, vcc quad_perm:[1,0,3,2] row_mask:0xf bank_mask:0xf
	v_cndmask_b32_dpp v155, v159, v155, vcc quad_perm:[1,0,3,2] row_mask:0xf bank_mask:0xf
	v_cndmask_b32_dpp v163, v167, v163, vcc quad_perm:[1,0,3,2] row_mask:0xf bank_mask:0xf
	v_cndmask_b32_dpp v156, v160, v156, vcc quad_perm:[1,0,3,2] row_mask:0xf bank_mask:0xf
	v_cndmask_b32_dpp v164, v168, v164, vcc quad_perm:[1,0,3,2] row_mask:0xf bank_mask:0xf
	v_cndmask_b32_dpp v157, v161, v157, vcc quad_perm:[1,0,3,2] row_mask:0xf bank_mask:0xf
	v_cndmask_b32_dpp v165, v169, v165, vcc quad_perm:[1,0,3,2] row_mask:0xf bank_mask:0xf
	s_mov_b32 vcc_lo, 0xcccccccc
	s_mov_b32 vcc_hi, 0xcccccccc
	s_nop 1
	v_cndmask_b32_dpp v158, v154, v162, vcc quad_perm:[2,3,0,1] row_mask:0xf bank_mask:0xf
	v_cndmask_b32_dpp v166, v170, v174, vcc quad_perm:[2,3,0,1] row_mask:0xf bank_mask:0xf
	v_cndmask_b32_dpp v159, v155, v163, vcc quad_perm:[2,3,0,1] row_mask:0xf bank_mask:0xf
	v_cndmask_b32_dpp v167, v171, v175, vcc quad_perm:[2,3,0,1] row_mask:0xf bank_mask:0xf
	v_cndmask_b32_dpp v160, v156, v164, vcc quad_perm:[2,3,0,1] row_mask:0xf bank_mask:0xf
	v_cndmask_b32_dpp v168, v172, v176, vcc quad_perm:[2,3,0,1] row_mask:0xf bank_mask:0xf
	v_cndmask_b32_dpp v161, v157, v165, vcc quad_perm:[2,3,0,1] row_mask:0xf bank_mask:0xf
	v_cndmask_b32_dpp v169, v173, v177, vcc quad_perm:[2,3,0,1] row_mask:0xf bank_mask:0xf
	s_mov_b32 vcc_lo, 0x33333333
	s_mov_b32 vcc_hi, 0x33333333
	s_nop 1
	v_cndmask_b32_dpp v154, v162, v154, vcc quad_perm:[2,3,0,1] row_mask:0xf bank_mask:0xf
	v_cndmask_b32_dpp v170, v174, v170, vcc quad_perm:[2,3,0,1] row_mask:0xf bank_mask:0xf
	v_cndmask_b32_dpp v155, v163, v155, vcc quad_perm:[2,3,0,1] row_mask:0xf bank_mask:0xf
	v_cndmask_b32_dpp v171, v175, v171, vcc quad_perm:[2,3,0,1] row_mask:0xf bank_mask:0xf
	v_cndmask_b32_dpp v156, v164, v156, vcc quad_perm:[2,3,0,1] row_mask:0xf bank_mask:0xf
	v_cndmask_b32_dpp v172, v176, v172, vcc quad_perm:[2,3,0,1] row_mask:0xf bank_mask:0xf
	v_cndmask_b32_dpp v157, v165, v157, vcc quad_perm:[2,3,0,1] row_mask:0xf bank_mask:0xf
	v_cndmask_b32_dpp v173, v177, v173, vcc quad_perm:[2,3,0,1] row_mask:0xf bank_mask:0xf
	global_store_dwordx4 v179, v[154:157], s[82:83] nt
	global_store_dwordx4 v180, v[170:173], s[82:83] nt
	global_store_dwordx4 v181, v[158:161], s[82:83] nt
	global_store_dwordx4 v190, v[166:169], s[82:83] nt
	v_readlane_b32 s2, v239, 0
	s_lshr_b32 s2, s2, 6
	s_add_i32 s2, s2, 6
	s_cmp_gt_u32 s2, 13
	s_cbranch_scc1 .Lhw_seam3_done
	s_add_i32 s2, s2, 56
	s_mul_i32 s2, s2, s74
	v_readlane_b32 s9, v239, 23
	s_lshr_b32 s9, s9, 3
	s_add_i32 s2, s2, s9
	s_cmp_gt_u32 s2, 24575
	s_cbranch_scc1 .Lhw_seam3_done
	v_mbcnt_lo_u32_b32 v178, -1, 0
	v_mbcnt_hi_u32_b32 v178, -1, v178
	v_and_b32_e32 v179, 60, v178
	v_lshlrev_b32_e32 v179, 10, v179
	v_and_b32_e32 v180, 3, v178
	v_lshl_or_b32 v179, v180, 4, v179
	v_add_u32_e32 v180, 0x400, v179
	v_add_u32_e32 v181, 0x800, v179
	v_add_u32_e32 v190, 0xc00, v179
	v_lshlrev_b32_e32 v178, 2, v178
	s_cmp_lt_u32 s2, 16384
	s_cbranch_scc0 .Lhw_dn_s3_1
	s_lshr_b32 s9, s2, 9
	s_bfe_u32 s32, s2, 0x40005
	s_and_b32 s53, s2, 31
	s_lshl_b32 s69, s9, 23
	s_lshl_b32 s100, s32, 19
	s_add_i32 s69, s69, s100
	s_lshl_b32 s100, s53, 8
	s_add_i32 s69, s69, s100
	s_lshl_b32 s98, s9, 11
	s_bfe_u32 s100, s53, 0x30001
	s_lshl_b32 s100, s100, 8
	s_add_i32 s98, s98, s100
	s_lshr_b32 s100, s53, 4
	s_lshl_b32 s100, s100, 7
	s_add_i32 s98, s98, s100
	s_and_b32 s100, s53, 1
	s_lshl_b32 s100, s100, 6
	s_add_i32 s98, s98, s100
	s_lshl_b32 s98, s98, 10
	s_lshl_b32 s100, s32, 6
	s_add_i32 s98, s98, s100
	s_add_i32 s98, s98, 0x2000000
	v_readlane_b32 s82, v239, 11
	v_readlane_b32 s83, v239, 12
	s_movk_i32 s89, 8192
	s_branch .Lhw_go_s3_1

.Lhw_seam4:
	s_mov_b64 exec, -1
	v_readlane_b32 s2, v239, 0
	s_lshr_b32 s2, s2, 6
	s_add_i32 s2, s2, -1
	s_cmp_gt_u32 s2, 13
	s_cbranch_scc1 .Lhw_seam4_done
	s_add_i32 s2, s2, 70
	s_mul_i32 s2, s2, s74
	v_readlane_b32 s9, v239, 23
	s_lshr_b32 s9, s9, 3
	s_add_i32 s2, s2, s9
	s_cmp_gt_u32 s2, 24575
	s_cbranch_scc1 .Lhw_seam4_done
	v_mbcnt_lo_u32_b32 v178, -1, 0
	v_mbcnt_hi_u32_b32 v178, -1, v178
	v_and_b32_e32 v179, 60, v178
	v_lshlrev_b32_e32 v179, 10, v179
	v_and_b32_e32 v180, 3, v178
	v_lshl_or_b32 v179, v180, 4, v179
	v_add_u32_e32 v180, 0x400, v179
	v_add_u32_e32 v181, 0x800, v179
	v_add_u32_e32 v190, 0xc00, v179
	v_lshlrev_b32_e32 v178, 2, v178
	s_cmp_lt_u32 s2, 16384
	s_cbranch_scc0 .Lhw_dn_s4_0
	s_lshr_b32 s9, s2, 9
	s_bfe_u32 s32, s2, 0x40005
	s_and_b32 s53, s2, 31
	s_lshl_b32 s69, s9, 23
	s_lshl_b32 s100, s32, 19
	s_add_i32 s69, s69, s100
	s_lshl_b32 s100, s53, 8
	s_add_i32 s69, s69, s100
	s_lshl_b32 s98, s9, 11
	s_bfe_u32 s100, s53, 0x30001
	s_lshl_b32 s100, s100, 8
	s_add_i32 s98, s98, s100
	s_lshr_b32 s100, s53, 4
	s_lshl_b32 s100, s100, 7
	s_add_i32 s98, s98, s100
	s_and_b32 s100, s53, 1
	s_lshl_b32 s100, s100, 6
	s_add_i32 s98, s98, s100
	s_lshl_b32 s98, s98, 10
	s_lshl_b32 s100, s32, 6
	s_add_i32 s98, s98, s100
	s_add_i32 s98, s98, 0x2000000
	v_readlane_b32 s82, v239, 11
	v_readlane_b32 s83, v239, 12
	s_movk_i32 s89, 8192
	s_branch .Lhw_go_s4_0

.Lhw_go_s4_0:
	s_add_u32 s100, s82, s69
	s_addc_u32 s101, s83, 0
	v_readlane_b32 s82, v239, 44
	v_readlane_b32 s83, v239, 45
	s_add_u32 s82, s82, s98
	s_addc_u32 s83, s83, 0
	global_load_dword v34, v178, s[100:101] nt
	s_add_u32 s100, s100, s89
	s_addc_u32 s101, s101, 0
	global_load_dword v35, v178, s[100:101] nt
	s_add_u32 s100, s100, s89
	s_addc_u32 s101, s101, 0
	global_load_dword v36, v178, s[100:101] nt
	s_add_u32 s100, s100, s89
	s_addc_u32 s101, s101, 0
	global_load_dword v37, v178, s[100:101] nt
	s_add_u32 s100, s100, s89
	s_addc_u32 s101, s101, 0
	global_load_dword v38, v178, s[100:101] nt
	s_add_u32 s100, s100, s89
	s_addc_u32 s101, s101, 0
	global_load_dword v39, v178, s[100:101] nt
	s_add_u32 s100, s100, s89
	s_addc_u32 s101, s101, 0
	global_load_dword v40, v178, s[100:101] nt
	s_add_u32 s100, s100, s89
	s_addc_u32 s101, s101, 0
	global_load_dword v41, v178, s[100:101] nt
	s_add_u32 s100, s100, s89
	s_addc_u32 s101, s101, 0
	global_load_dword v42, v178, s[100:101] nt
	s_add_u32 s100, s100, s89
	s_addc_u32 s101, s101, 0
	global_load_dword v43, v178, s[100:101] nt
	s_add_u32 s100, s100, s89
	s_addc_u32 s101, s101, 0
	global_load_dword v44, v178, s[100:101] nt
	s_add_u32 s100, s100, s89
	s_addc_u32 s101, s101, 0
	global_load_dword v45, v178, s[100:101] nt
	s_add_u32 s100, s100, s89
	s_addc_u32 s101, s101, 0
	global_load_dword v46, v178, s[100:101] nt
	s_add_u32 s100, s100, s89
	s_addc_u32 s101, s101, 0
	global_load_dword v47, v178, s[100:101] nt
	s_add_u32 s100, s100, s89
	s_addc_u32 s101, s101, 0
	global_load_dword v48, v178, s[100:101] nt
	s_add_u32 s100, s100, s89
	s_addc_u32 s101, s101, 0
	global_load_dword v49, v178, s[100:101] nt
	s_add_u32 s100, s100, s89
	s_addc_u32 s101, s101, 0
	global_load_dword v50, v178, s[100:101] nt
	s_add_u32 s100, s100, s89
	s_addc_u32 s101, s101, 0
	global_load_dword v51, v178, s[100:101] nt
	s_add_u32 s100, s100, s89
	s_addc_u32 s101, s101, 0
	global_load_dword v52, v178, s[100:101] nt
	s_add_u32 s100, s100, s89
	s_addc_u32 s101, s101, 0
	global_load_dword v53, v178, s[100:101] nt
	s_add_u32 s100, s100, s89
	s_addc_u32 s101, s101, 0
	global_load_dword v54, v178, s[100:101] nt
	s_add_u32 s100, s100, s89
	s_addc_u32 s101, s101, 0
	global_load_dword v55, v178, s[100:101] nt
	s_add_u32 s100, s100, s89
	s_addc_u32 s101, s101, 0
	global_load_dword v56, v178, s[100:101] nt
	s_add_u32 s100, s100, s89
	s_addc_u32 s101, s101, 0
	global_load_dword v57, v178, s[100:101] nt
	s_add_u32 s100, s100, s89
	s_addc_u32 s101, s101, 0
	global_load_dword v58, v178, s[100:101] nt
	s_add_u32 s100, s100, s89
	s_addc_u32 s101, s101, 0
	global_load_dword v59, v178, s[100:101] nt
	s_add_u32 s100, s100, s89
	s_addc_u32 s101, s101, 0
	global_load_dword v60, v178, s[100:101] nt
	s_add_u32 s100, s100, s89
	s_addc_u32 s101, s101, 0
	global_load_dword v61, v178, s[100:101] nt
	s_add_u32 s100, s100, s89
	s_addc_u32 s101, s101, 0
	global_load_dword v62, v178, s[100:101] nt
	s_add_u32 s100, s100, s89
	s_addc_u32 s101, s101, 0
	global_load_dword v63, v178, s[100:101] nt
	s_add_u32 s100, s100, s89
	s_addc_u32 s101, s101, 0
	global_load_dword v64, v178, s[100:101] nt
	s_add_u32 s100, s100, s89
	s_addc_u32 s101, s101, 0
	global_load_dword v65, v178, s[100:101] nt
	s_add_u32 s100, s100, s89
	s_addc_u32 s101, s101, 0
	global_load_dword v66, v178, s[100:101] nt
	s_add_u32 s100, s100, s89
	s_addc_u32 s101, s101, 0
	global_load_dword v67, v178, s[100:101] nt
	s_add_u32 s100, s100, s89
	s_addc_u32 s101, s101, 0
	global_load_dword v68, v178, s[100:101] nt
	s_add_u32 s100, s100, s89
	s_addc_u32 s101, s101, 0
	global_load_dword v69, v178, s[100:101] nt
	s_add_u32 s100, s100, s89
	s_addc_u32 s101, s101, 0
	global_load_dword v70, v178, s[100:101] nt
	s_add_u32 s100, s100, s89
	s_addc_u32 s101, s101, 0
	global_load_dword v71, v178, s[100:101] nt
	s_add_u32 s100, s100, s89
	s_addc_u32 s101, s101, 0
	global_load_dword v72, v178, s[100:101] nt
	s_add_u32 s100, s100, s89
	s_addc_u32 s101, s101, 0
	global_load_dword v73, v178, s[100:101] nt
	s_add_u32 s100, s100, s89
	s_addc_u32 s101, s101, 0
	global_load_dword v74, v178, s[100:101] nt
	s_add_u32 s100, s100, s89
	s_addc_u32 s101, s101, 0
	global_load_dword v75, v178, s[100:101] nt
	s_add_u32 s100, s100, s89
	s_addc_u32 s101, s101, 0
	global_load_dword v76, v178, s[100:101] nt
	s_add_u32 s100, s100, s89
	s_addc_u32 s101, s101, 0
	global_load_dword v77, v178, s[100:101] nt
	s_add_u32 s100, s100, s89
	s_addc_u32 s101, s101, 0
	global_load_dword v78, v178, s[100:101] nt
	s_add_u32 s100, s100, s89
	s_addc_u32 s101, s101, 0
	global_load_dword v79, v178, s[100:101] nt
	s_add_u32 s100, s100, s89
	s_addc_u32 s101, s101, 0
	global_load_dword v80, v178, s[100:101] nt
	s_add_u32 s100, s100, s89
	s_addc_u32 s101, s101, 0
	global_load_dword v81, v178, s[100:101] nt
	s_add_u32 s100, s100, s89
	s_addc_u32 s101, s101, 0
	global_load_dword v82, v178, s[100:101] nt
	s_add_u32 s100, s100, s89
	s_addc_u32 s101, s101, 0
	global_load_dword v83, v178, s[100:101] nt
	s_add_u32 s100, s100, s89
	s_addc_u32 s101, s101, 0
	global_load_dword v84, v178, s[100:101] nt
	s_add_u32 s100, s100, s89
	s_addc_u32 s101, s101, 0
	global_load_dword v85, v178, s[100:101] nt
	s_add_u32 s100, s100, s89
	s_addc_u32 s101, s101, 0
	global_load_dword v86, v178, s[100:101] nt
	s_add_u32 s100, s100, s89
	s_addc_u32 s101, s101, 0
	global_load_dword v87, v178, s[100:101] nt
	s_add_u32 s100, s100, s89
	s_addc_u32 s101, s101, 0
	global_load_dword v88, v178, s[100:101] nt
	s_add_u32 s100, s100, s89
	s_addc_u32 s101, s101, 0
	global_load_dword v89, v178, s[100:101] nt
	s_add_u32 s100, s100, s89
	s_addc_u32 s101, s101, 0
	global_load_dword v90, v178, s[100:101] nt
	s_add_u32 s100, s100, s89
	s_addc_u32 s101, s101, 0
	global_load_dword v91, v178, s[100:101] nt
	s_add_u32 s100, s100, s89
	s_addc_u32 s101, s101, 0
	global_load_dword v92, v178, s[100:101] nt
	s_add_u32 s100, s100, s89
	s_addc_u32 s101, s101, 0
	global_load_dword v93, v178, s[100:101] nt
	s_add_u32 s100, s100, s89
	s_addc_u32 s101, s101, 0
	global_load_dword v94, v178, s[100:101] nt
	s_add_u32 s100, s100, s89
	s_addc_u32 s101, s101, 0
	global_load_dword v95, v178, s[100:101] nt
	s_add_u32 s100, s100, s89
	s_addc_u32 s101, s101, 0
	global_load_dword v96, v178, s[100:101] nt
	s_add_u32 s100, s100, s89
	s_addc_u32 s101, s101, 0
	global_load_dword v97, v178, s[100:101] nt
	s_add_u32 s100, s100, s89
	s_addc_u32 s101, s101, 0
	s_waitcnt vmcnt(48)
	v_mul_f32_e32 v34, 0x42000000, v34
	v_mul_f32_e32 v35, 0x42000000, v35
	v_mul_f32_e32 v36, 0x42000000, v36
	v_mul_f32_e32 v37, 0x42000000, v37
	v_mul_f32_e32 v38, 0x42000000, v38
	v_mul_f32_e32 v39, 0x42000000, v39
	v_mul_f32_e32 v40, 0x42000000, v40
	v_mul_f32_e32 v41, 0x42000000, v41
	v_mul_f32_e32 v42, 0x42000000, v42
	v_mul_f32_e32 v43, 0x42000000, v43
	v_mul_f32_e32 v44, 0x42000000, v44
	v_mul_f32_e32 v45, 0x42000000, v45
	v_mul_f32_e32 v46, 0x42000000, v46
	v_mul_f32_e32 v47, 0x42000000, v47
	v_mul_f32_e32 v48, 0x42000000, v48
	v_mul_f32_e32 v49, 0x42000000, v49
	v_cvt_pk_fp8_f32 v154, v34, v35
	v_cvt_pk_fp8_f32 v155, v38, v39
	v_cvt_pk_fp8_f32 v156, v42, v43
	v_cvt_pk_fp8_f32 v157, v46, v47
	v_cvt_pk_fp8_f32 v154, v36, v37 op_sel:[0,0,1]
	v_cvt_pk_fp8_f32 v155, v40, v41 op_sel:[0,0,1]
	v_cvt_pk_fp8_f32 v156, v44, v45 op_sel:[0,0,1]
	v_cvt_pk_fp8_f32 v157, v48, v49 op_sel:[0,0,1]
	s_waitcnt vmcnt(32)
	v_mul_f32_e32 v50, 0x42000000, v50
	v_mul_f32_e32 v51, 0x42000000, v51
	v_mul_f32_e32 v52, 0x42000000, v52
	v_mul_f32_e32 v53, 0x42000000, v53
	v_mul_f32_e32 v54, 0x42000000, v54
	v_mul_f32_e32 v55, 0x42000000, v55
	v_mul_f32_e32 v56, 0x42000000, v56
	v_mul_f32_e32 v57, 0x42000000, v57
	v_mul_f32_e32 v58, 0x42000000, v58
	v_mul_f32_e32 v59, 0x42000000, v59
	v_mul_f32_e32 v60, 0x42000000, v60
	v_mul_f32_e32 v61, 0x42000000, v61
	v_mul_f32_e32 v62, 0x42000000, v62
	v_mul_f32_e32 v63, 0x42000000, v63
	v_mul_f32_e32 v64, 0x42000000, v64
	v_mul_f32_e32 v65, 0x42000000, v65
	v_cvt_pk_fp8_f32 v158, v50, v51
	v_cvt_pk_fp8_f32 v159, v54, v55
	v_cvt_pk_fp8_f32 v160, v58, v59
	v_cvt_pk_fp8_f32 v161, v62, v63
	v_cvt_pk_fp8_f32 v158, v52, v53 op_sel:[0,0,1]
	v_cvt_pk_fp8_f32 v159, v56, v57 op_sel:[0,0,1]
	v_cvt_pk_fp8_f32 v160, v60, v61 op_sel:[0,0,1]
	v_cvt_pk_fp8_f32 v161, v64, v65 op_sel:[0,0,1]
	s_waitcnt vmcnt(16)
	v_mul_f32_e32 v66, 0x42000000, v66
	v_mul_f32_e32 v67, 0x42000000, v67
	v_mul_f32_e32 v68, 0x42000000, v68
	v_mul_f32_e32 v69, 0x42000000, v69
	v_mul_f32_e32 v70, 0x42000000, v70
	v_mul_f32_e32 v71, 0x42000000, v71
	v_mul_f32_e32 v72, 0x42000000, v72
	v_mul_f32_e32 v73, 0x42000000, v73
	v_mul_f32_e32 v74, 0x42000000, v74
	v_mul_f32_e32 v75, 0x42000000, v75
	v_mul_f32_e32 v76, 0x42000000, v76
	v_mul_f32_e32 v77, 0x42000000, v77
	v_mul_f32_e32 v78, 0x42000000, v78
	v_mul_f32_e32 v79, 0x42000000, v79
	v_mul_f32_e32 v80, 0x42000000, v80
	v_mul_f32_e32 v81, 0x42000000, v81
	v_cvt_pk_fp8_f32 v162, v66, v67
	v_cvt_pk_fp8_f32 v163, v70, v71
	v_cvt_pk_fp8_f32 v164, v74, v75
	v_cvt_pk_fp8_f32 v165, v78, v79
	v_cvt_pk_fp8_f32 v162, v68, v69 op_sel:[0,0,1]
	v_cvt_pk_fp8_f32 v163, v72, v73 op_sel:[0,0,1]
	v_cvt_pk_fp8_f32 v164, v76, v77 op_sel:[0,0,1]
	v_cvt_pk_fp8_f32 v165, v80, v81 op_sel:[0,0,1]
	s_waitcnt vmcnt(0)
	v_mul_f32_e32 v82, 0x42000000, v82
	v_mul_f32_e32 v83, 0x42000000, v83
	v_mul_f32_e32 v84, 0x42000000, v84
	v_mul_f32_e32 v85, 0x42000000, v85
	v_mul_f32_e32 v86, 0x42000000, v86
	v_mul_f32_e32 v87, 0x42000000, v87
	v_mul_f32_e32 v88, 0x42000000, v88
	v_mul_f32_e32 v89, 0x42000000, v89
	v_mul_f32_e32 v90, 0x42000000, v90
	v_mul_f32_e32 v91, 0x42000000, v91
	v_mul_f32_e32 v92, 0x42000000, v92
	v_mul_f32_e32 v93, 0x42000000, v93
	v_mul_f32_e32 v94, 0x42000000, v94
	v_mul_f32_e32 v95, 0x42000000, v95
	v_mul_f32_e32 v96, 0x42000000, v96
	v_mul_f32_e32 v97, 0x42000000, v97
	v_cvt_pk_fp8_f32 v166, v82, v83
	v_cvt_pk_fp8_f32 v167, v86, v87
	v_cvt_pk_fp8_f32 v168, v90, v91
	v_cvt_pk_fp8_f32 v169, v94, v95
	v_cvt_pk_fp8_f32 v166, v84, v85 op_sel:[0,0,1]
	v_cvt_pk_fp8_f32 v167, v88, v89 op_sel:[0,0,1]
	v_cvt_pk_fp8_f32 v168, v92, v93 op_sel:[0,0,1]
	v_cvt_pk_fp8_f32 v169, v96, v97 op_sel:[0,0,1]
	s_mov_b32 vcc_lo, 0xaaaaaaaa
	s_mov_b32 vcc_hi, 0xaaaaaaaa
	s_nop 1
	v_cndmask_b32_dpp v170, v154, v158, vcc quad_perm:[1,0,3,2] row_mask:0xf bank_mask:0xf
	v_cndmask_b32_dpp v174, v162, v166, vcc quad_perm:[1,0,3,2] row_mask:0xf bank_mask:0xf
	v_cndmask_b32_dpp v171, v155, v159, vcc quad_perm:[1,0,3,2] row_mask:0xf bank_mask:0xf
	v_cndmask_b32_dpp v175, v163, v167, vcc quad_perm:[1,0,3,2] row_mask:0xf bank_mask:0xf
	v_cndmask_b32_dpp v172, v156, v160, vcc quad_perm:[1,0,3,2] row_mask:0xf bank_mask:0xf
	v_cndmask_b32_dpp v176, v164, v168, vcc quad_perm:[1,0,3,2] row_mask:0xf bank_mask:0xf
	v_cndmask_b32_dpp v173, v157, v161, vcc quad_perm:[1,0,3,2] row_mask:0xf bank_mask:0xf
	v_cndmask_b32_dpp v177, v165, v169, vcc quad_perm:[1,0,3,2] row_mask:0xf bank_mask:0xf
	s_mov_b32 vcc_lo, 0x55555555
	s_mov_b32 vcc_hi, 0x55555555
	s_nop 1
	v_cndmask_b32_dpp v154, v158, v154, vcc quad_perm:[1,0,3,2] row_mask:0xf bank_mask:0xf
	v_cndmask_b32_dpp v162, v166, v162, vcc quad_perm:[1,0,3,2] row_mask:0xf bank_mask:0xf
	v_cndmask_b32_dpp v155, v159, v155, vcc quad_perm:[1,0,3,2] row_mask:0xf bank_mask:0xf
	v_cndmask_b32_dpp v163, v167, v163, vcc quad_perm:[1,0,3,2] row_mask:0xf bank_mask:0xf
	v_cndmask_b32_dpp v156, v160, v156, vcc quad_perm:[1,0,3,2] row_mask:0xf bank_mask:0xf
	v_cndmask_b32_dpp v164, v168, v164, vcc quad_perm:[1,0,3,2] row_mask:0xf bank_mask:0xf
	v_cndmask_b32_dpp v157, v161, v157, vcc quad_perm:[1,0,3,2] row_mask:0xf bank_mask:0xf
	v_cndmask_b32_dpp v165, v169, v165, vcc quad_perm:[1,0,3,2] row_mask:0xf bank_mask:0xf
	s_mov_b32 vcc_lo, 0xcccccccc
	s_mov_b32 vcc_hi, 0xcccccccc
	s_nop 1
	v_cndmask_b32_dpp v158, v154, v162, vcc quad_perm:[2,3,0,1] row_mask:0xf bank_mask:0xf
	v_cndmask_b32_dpp v166, v170, v174, vcc quad_perm:[2,3,0,1] row_mask:0xf bank_mask:0xf
	v_cndmask_b32_dpp v159, v155, v163, vcc quad_perm:[2,3,0,1] row_mask:0xf bank_mask:0xf
	v_cndmask_b32_dpp v167, v171, v175, vcc quad_perm:[2,3,0,1] row_mask:0xf bank_mask:0xf
	v_cndmask_b32_dpp v160, v156, v164, vcc quad_perm:[2,3,0,1] row_mask:0xf bank_mask:0xf
	v_cndmask_b32_dpp v168, v172, v176, vcc quad_perm:[2,3,0,1] row_mask:0xf bank_mask:0xf
	v_cndmask_b32_dpp v161, v157, v165, vcc quad_perm:[2,3,0,1] row_mask:0xf bank_mask:0xf
	v_cndmask_b32_dpp v169, v173, v177, vcc quad_perm:[2,3,0,1] row_mask:0xf bank_mask:0xf
	s_mov_b32 vcc_lo, 0x33333333
	s_mov_b32 vcc_hi, 0x33333333
	s_nop 1
	v_cndmask_b32_dpp v154, v162, v154, vcc quad_perm:[2,3,0,1] row_mask:0xf bank_mask:0xf
	v_cndmask_b32_dpp v170, v174, v170, vcc quad_perm:[2,3,0,1] row_mask:0xf bank_mask:0xf
	v_cndmask_b32_dpp v155, v163, v155, vcc quad_perm:[2,3,0,1] row_mask:0xf bank_mask:0xf
	v_cndmask_b32_dpp v171, v175, v171, vcc quad_perm:[2,3,0,1] row_mask:0xf bank_mask:0xf
	v_cndmask_b32_dpp v156, v164, v156, vcc quad_perm:[2,3,0,1] row_mask:0xf bank_mask:0xf
	v_cndmask_b32_dpp v172, v176, v172, vcc quad_perm:[2,3,0,1] row_mask:0xf bank_mask:0xf
	v_cndmask_b32_dpp v157, v165, v157, vcc quad_perm:[2,3,0,1] row_mask:0xf bank_mask:0xf
	v_cndmask_b32_dpp v173, v177, v173, vcc quad_perm:[2,3,0,1] row_mask:0xf bank_mask:0xf
	global_store_dwordx4 v179, v[154:157], s[82:83] nt
	global_store_dwordx4 v180, v[170:173], s[82:83] nt
	global_store_dwordx4 v181, v[158:161], s[82:83] nt
	global_store_dwordx4 v190, v[166:169], s[82:83] nt
	v_readlane_b32 s2, v239, 0
	s_lshr_b32 s2, s2, 6
	s_add_i32 s2, s2, 6
	s_cmp_gt_u32 s2, 13
	s_cbranch_scc1 .Lhw_seam4_done
	s_add_i32 s2, s2, 70
	s_mul_i32 s2, s2, s74
	v_readlane_b32 s9, v239, 23
	s_lshr_b32 s9, s9, 3
	s_add_i32 s2, s2, s9
	s_cmp_gt_u32 s2, 24575
	s_cbranch_scc1 .Lhw_seam4_done
	v_mbcnt_lo_u32_b32 v178, -1, 0
	v_mbcnt_hi_u32_b32 v178, -1, v178
	v_and_b32_e32 v179, 60, v178
	v_lshlrev_b32_e32 v179, 10, v179
	v_and_b32_e32 v180, 3, v178
	v_lshl_or_b32 v179, v180, 4, v179
	v_add_u32_e32 v180, 0x400, v179
	v_add_u32_e32 v181, 0x800, v179
	v_add_u32_e32 v190, 0xc00, v179
	v_lshlrev_b32_e32 v178, 2, v178
	s_cmp_lt_u32 s2, 16384
	s_cbranch_scc0 .Lhw_dn_s4_1
	s_lshr_b32 s9, s2, 9
	s_bfe_u32 s32, s2, 0x40005
	s_and_b32 s53, s2, 31
	s_lshl_b32 s69, s9, 23
	s_lshl_b32 s100, s32, 19
	s_add_i32 s69, s69, s100
	s_lshl_b32 s100, s53, 8
	s_add_i32 s69, s69, s100
	s_lshl_b32 s98, s9, 11
	s_bfe_u32 s100, s53, 0x30001
	s_lshl_b32 s100, s100, 8
	s_add_i32 s98, s98, s100
	s_lshr_b32 s100, s53, 4
	s_lshl_b32 s100, s100, 7
	s_add_i32 s98, s98, s100
	s_and_b32 s100, s53, 1
	s_lshl_b32 s100, s100, 6
	s_add_i32 s98, s98, s100
	s_lshl_b32 s98, s98, 10
	s_lshl_b32 s100, s32, 6
	s_add_i32 s98, s98, s100
	s_add_i32 s98, s98, 0x2000000
	v_readlane_b32 s82, v239, 11
	v_readlane_b32 s83, v239, 12
	s_movk_i32 s89, 8192
	s_branch .Lhw_go_s4_1
